# attention loop: packed row-sum accumulators restart from the first words after a flush (4 VALU fewer per flush), loop exit test moved ahead of the closing barrier
# speedup vs baseline: 1.0124x; 1.0036x over previous
.LBB0_336:
	ds_read_b64_tr_b16 v[144:145], v211 offset:49152
	ds_read_b64_tr_b16 v[146:147], v211 offset:49664
	s_waitcnt lgkmcnt(9)
	v_mfma_f32_32x32x16_bf16 v[84:99], v[68:71], v[140:143], -4.0
	v_pk_add_f16 v0, v72, v150
	v_pk_add_f16 v68, v73, v151
	v_cvt_pk_f16_f32 v124, v52, v53
	v_pk_add_f16 v0, v0, v68
	v_cvt_pk_f16_f32 v125, v54, v55
	v_dot2c_f32_f16_e32 v2, 0x3c003c00, v0
	ds_read_b64_tr_b16 v[52:53], v211 offset:53248
	ds_read_b64_tr_b16 v[54:55], v211 offset:53760
	s_waitcnt lgkmcnt(10)
	v_mfma_f32_32x32x16_bf16 v[68:83], v[160:163], v[140:143], -4.0
	v_exp_f32_e32 v44, v44
	v_cvt_pk_f16_f32 v126, v56, v57
	v_cvt_pk_f16_f32 v127, v58, v59
	ds_read_b64_tr_b16 v[56:57], v211 offset:50176
	ds_read_b64_tr_b16 v[58:59], v211 offset:50688
	s_waitcnt lgkmcnt(11)
	v_mfma_f32_32x32x16_bf16 v[84:99], v[156:159], v[128:131], v[84:99]
	v_exp_f32_e32 v45, v45
	v_pk_add_f16 v0, v124, v126
	v_pk_add_f16 v116, v125, v127
	v_cvt_pk_f16_f32 v120, v60, v61
	v_cvt_pk_f16_f32 v121, v62, v63
	ds_read_b64_tr_b16 v[60:61], v211 offset:54272
	ds_read_b64_tr_b16 v[62:63], v211 offset:54784
	s_waitcnt lgkmcnt(12)
	v_mfma_f32_32x32x16_bf16 v[68:83], v[112:115], v[128:131], v[68:83]
	v_exp_f32_e32 v46, v46
	v_exp_f32_e32 v47, v47
	v_pk_add_f16 v0, v0, v120
	v_pk_add_f16 v116, v116, v121
	v_cvt_pk_f16_f32 v122, v64, v65
	v_cvt_pk_f16_f32 v123, v66, v67
	ds_read_b64_tr_b16 v[64:65], v211 offset:51200
	ds_read_b64_tr_b16 v[66:67], v211 offset:51712
	s_waitcnt lgkmcnt(13)
	v_mfma_f32_32x32x16_bf16 v[84:99], v[152:155], v[136:139], v[84:99]
	v_exp_f32_e32 v48, v48
	v_exp_f32_e32 v49, v49
	v_pk_add_f16 v0, v0, v122
	v_pk_add_f16 v112, v116, v123
	v_cvt_pk_f16_f32 v116, v36, v37
	v_cvt_pk_f16_f32 v117, v38, v39
	ds_read_b64_tr_b16 v[36:37], v211 offset:55296
	ds_read_b64_tr_b16 v[38:39], v211 offset:55808
	s_waitcnt lgkmcnt(14)
	v_mfma_f32_32x32x16_bf16 v[68:83], v[104:107], v[136:139], v[68:83]
	v_exp_f32_e32 v50, v50
	v_pk_add_f16 v0, v0, v116
	v_pk_add_f16 v112, v112, v117
	v_cvt_pk_f16_f32 v118, v40, v41
	v_cvt_pk_f16_f32 v119, v42, v43
	ds_read_b64_tr_b16 v[40:41], v211 offset:52224
	ds_read_b64_tr_b16 v[42:43], v211 offset:52736
	v_cvt_pk_f16_f32 v148, v44, v45
	v_pk_add_f16 v0, v0, v118
	v_pk_add_f16 v104, v112, v119
	v_cvt_pk_f16_f32 v149, v46, v47
	s_waitcnt lgkmcnt(14)
	v_mfma_f32_32x32x16_bf16 v[84:99], v[108:111], v[132:135], v[84:99]
	v_exp_f32_e32 v51, v51
	ds_read_b64_tr_b16 v[44:45], v211 offset:56320
	ds_read_b64_tr_b16 v[46:47], v211 offset:56832
	v_mfma_f32_32x32x16_bf16 v[68:83], v[100:103], v[132:135], v[68:83]
	v_pk_add_f16 v0, v0, v148
	v_pk_add_f16 v166, v104, v149
	v_cvt_pk_f16_f32 v150, v48, v49
	v_cvt_pk_f16_f32 v151, v50, v51
	s_add_u32 s56, s88, s54
	s_addc_u32 s57, s89, s55
	s_add_u32 s58, s56, 0x48000
	s_addc_u32 s59, s57, 0
	s_mov_b32 m0, s70
	s_nop 0
	global_load_lds_dwordx4 v165, s[58:59]
	s_add_u32 s58, s14, s54
	s_addc_u32 s59, s15, s55
	s_add_u32 s62, s58, 0x30000
	s_addc_u32 s63, s59, 0
	s_cmp_lg_u32 0, -1
	s_cselect_b32 s60, 0, 0
	s_add_i32 s60, s60, s44
	s_add_i32 s61, s60, 0x14000
	s_mov_b32 m0, s61
	s_nop 0
	global_load_lds_dwordx4 v164, s[62:63]
	s_waitcnt lgkmcnt(14)
	v_mfma_f32_32x32x16_f16 v[4:19], v[124:127], v[144:147], v[4:19]
	v_exp_f32_e32 v84, v84
	v_exp_f32_e32 v85, v85
	v_exp_f32_e32 v86, v86
	s_waitcnt lgkmcnt(12)
	v_mfma_f32_32x32x16_f16 v[20:35], v[124:127], v[52:55], v[20:35]
	v_exp_f32_e32 v87, v87
	v_exp_f32_e32 v88, v88
	v_exp_f32_e32 v89, v89
	ds_read_b128 v[48:51], v210 offset:16384
	ds_read_b128 v[52:55], v210 offset:16896
	s_waitcnt lgkmcnt(12)
	v_mfma_f32_32x32x16_f16 v[4:19], v[120:123], v[56:59], v[4:19]
	v_exp_f32_e32 v90, v90
	v_exp_f32_e32 v91, v91
	v_exp_f32_e32 v92, v92
	ds_read_b128 v[56:59], v210 offset:18432
	ds_read_b128 v[144:147], v210 offset:18944
	s_waitcnt lgkmcnt(12)
	v_mfma_f32_32x32x16_f16 v[20:35], v[120:123], v[60:63], v[20:35]
	v_exp_f32_e32 v93, v93
	v_exp_f32_e32 v94, v94
	v_exp_f32_e32 v95, v95
	ds_read_b128 v[60:63], v210 offset:20480
	ds_read_b128 v[152:155], v210 offset:20992
	s_waitcnt lgkmcnt(12)
	v_mfma_f32_32x32x16_f16 v[4:19], v[116:119], v[64:67], v[4:19]
	v_exp_f32_e32 v96, v96
	v_exp_f32_e32 v97, v97
	v_exp_f32_e32 v98, v98
	ds_read_b128 v[64:67], v210 offset:22528
	ds_read_b128 v[156:159], v210 offset:23040
	s_waitcnt lgkmcnt(12)
	v_mfma_f32_32x32x16_f16 v[20:35], v[116:119], v[36:39], v[20:35]
	v_exp_f32_e32 v99, v99
	v_exp_f32_e32 v68, v68
	v_exp_f32_e32 v69, v69
	s_waitcnt lgkmcnt(10)
	v_mfma_f32_32x32x16_f16 v[4:19], v[148:151], v[40:43], v[4:19]
	v_exp_f32_e32 v70, v70
	v_exp_f32_e32 v71, v71
	v_exp_f32_e32 v72, v72
	s_waitcnt lgkmcnt(8)
	v_mfma_f32_32x32x16_f16 v[20:35], v[148:151], v[44:47], v[20:35]
	v_exp_f32_e32 v73, v73
	v_exp_f32_e32 v74, v74
	v_exp_f32_e32 v75, v75
	ds_read_b64_tr_b16 v[160:161], v211 offset:57344
	ds_read_b64_tr_b16 v[162:163], v211 offset:57856
	s_waitcnt lgkmcnt(9)
	v_mfma_f32_32x32x16_bf16 v[100:115], v[48:51], v[140:143], -4.0
	v_exp_f32_e32 v76, v76
	v_cvt_pk_f16_f32 v124, v84, v85
	v_pk_add_f16 v0, v0, v150
	v_pk_add_f16 v116, v166, v151
	v_cvt_pk_f16_f32 v125, v86, v87
	ds_read_b64_tr_b16 v[84:85], v211 offset:61440
	ds_read_b64_tr_b16 v[86:87], v211 offset:61952
	s_waitcnt lgkmcnt(10)
	v_mfma_f32_32x32x16_bf16 v[36:51], v[52:55], v[140:143], -4.0
	v_exp_f32_e32 v77, v77
	v_pk_add_f16 v0, v0, v124
	v_pk_add_f16 v116, v116, v125
	v_cvt_pk_f16_f32 v126, v88, v89
	v_cvt_pk_f16_f32 v127, v90, v91
	ds_read_b64_tr_b16 v[52:53], v211 offset:58368
	ds_read_b64_tr_b16 v[54:55], v211 offset:58880
	s_waitcnt lgkmcnt(11)
	v_mfma_f32_32x32x16_bf16 v[100:115], v[56:59], v[128:131], v[100:115]
	v_exp_f32_e32 v78, v78
	v_cvt_pk_f16_f32 v120, v92, v93
	v_pk_add_f16 v0, v0, v126
	v_pk_add_f16 v88, v116, v127
	v_cvt_pk_f16_f32 v121, v94, v95
	ds_read_b64_tr_b16 v[56:57], v211 offset:62464
	ds_read_b64_tr_b16 v[58:59], v211 offset:62976
	s_waitcnt lgkmcnt(12)
	v_mfma_f32_32x32x16_bf16 v[36:51], v[144:147], v[128:131], v[36:51]
	v_exp_f32_e32 v79, v79
	v_exp_f32_e32 v80, v80
	v_pk_add_f16 v0, v0, v120
	v_pk_add_f16 v92, v88, v121
	v_cvt_pk_f16_f32 v122, v96, v97
	v_cvt_pk_f16_f32 v123, v98, v99
	ds_read_b64_tr_b16 v[88:89], v211 offset:59392
	ds_read_b64_tr_b16 v[90:91], v211 offset:59904
	s_waitcnt lgkmcnt(13)
	v_mfma_f32_32x32x16_bf16 v[100:115], v[60:63], v[136:139], v[100:115]
	v_exp_f32_e32 v81, v81
	v_cvt_pk_f16_f32 v116, v68, v69
	v_pk_add_f16 v0, v0, v122
	v_pk_add_f16 v92, v92, v123
	v_cvt_pk_f16_f32 v117, v70, v71
	ds_read_b64_tr_b16 v[60:61], v211 offset:63488
	ds_read_b64_tr_b16 v[62:63], v211 offset:64000
	s_waitcnt lgkmcnt(14)
	v_mfma_f32_32x32x16_bf16 v[36:51], v[152:155], v[136:139], v[36:51]
	v_exp_f32_e32 v82, v82
	v_pk_add_f16 v0, v0, v116
	v_pk_add_f16 v92, v92, v117
	v_cvt_pk_f16_f32 v118, v72, v73
	v_cvt_pk_f16_f32 v119, v74, v75
	ds_read_b64_tr_b16 v[68:69], v211 offset:60416
	ds_read_b64_tr_b16 v[70:71], v211 offset:60928
	s_waitcnt lgkmcnt(14)
	v_mfma_f32_32x32x16_bf16 v[100:115], v[64:67], v[132:135], v[100:115]
	v_exp_f32_e32 v83, v83
	v_cvt_pk_f16_f32 v148, v76, v77
	v_pk_add_f16 v0, v0, v118
	v_pk_add_f16 v72, v92, v119
	v_cvt_pk_f16_f32 v149, v78, v79
	ds_read_b64_tr_b16 v[64:65], v211 offset:64512
	ds_read_b64_tr_b16 v[66:67], v211 offset:65024
	v_mfma_f32_32x32x16_bf16 v[36:51], v[156:159], v[132:135], v[36:51]
	v_pk_add_f16 v0, v0, v148
	v_pk_add_f16 v170, v72, v149
	v_cvt_pk_f16_f32 v150, v80, v81
	v_cvt_pk_f16_f32 v151, v82, v83
	s_add_u32 s62, s56, 0x54000
	s_addc_u32 s63, s57, 0
	s_mov_b32 m0, s71
	s_nop 0
	global_load_lds_dwordx4 v165, s[62:63]
	s_add_u32 s62, s58, 0x3c000
	s_addc_u32 s63, s59, 0
	s_add_i32 s60, s60, 0x16000
	s_mov_b32 m0, s60
	s_nop 0
	global_load_lds_dwordx4 v164, s[62:63]
	s_waitcnt lgkmcnt(14)
	v_mfma_f32_32x32x16_f16 v[4:19], v[124:127], v[160:163], v[4:19]
	v_exp_f32_e32 v100, v100
	v_exp_f32_e32 v101, v101
	v_exp_f32_e32 v102, v102
	s_waitcnt lgkmcnt(12)
	v_mfma_f32_32x32x16_f16 v[20:35], v[124:127], v[84:87], v[20:35]
	v_exp_f32_e32 v103, v103
	v_exp_f32_e32 v104, v104
	v_exp_f32_e32 v105, v105
	ds_read_b128 v[92:95], v210 offset:24576
	ds_read_b128 v[96:99], v210 offset:25088
	s_waitcnt lgkmcnt(12)
	v_mfma_f32_32x32x16_f16 v[4:19], v[120:123], v[52:55], v[4:19]
	v_exp_f32_e32 v106, v106
	v_exp_f32_e32 v107, v107
	v_exp_f32_e32 v108, v108
	ds_read_b128 v[144:147], v210 offset:26624
	ds_read_b128 v[152:155], v210 offset:27136
	s_waitcnt lgkmcnt(12)
	v_mfma_f32_32x32x16_f16 v[20:35], v[120:123], v[56:59], v[20:35]
	v_exp_f32_e32 v109, v109
	v_exp_f32_e32 v110, v110
	v_exp_f32_e32 v111, v111
	ds_read_b128 v[156:159], v210 offset:28672
	ds_read_b128 v[160:163], v210 offset:29184
	s_waitcnt lgkmcnt(12)
	v_mfma_f32_32x32x16_f16 v[4:19], v[116:119], v[88:91], v[4:19]
	v_exp_f32_e32 v112, v112
	v_exp_f32_e32 v113, v113
	v_exp_f32_e32 v114, v114
	ds_read_b128 v[88:91], v210 offset:30720
	ds_read_b128 v[84:87], v210 offset:31232
	s_waitcnt lgkmcnt(12)
	v_mfma_f32_32x32x16_f16 v[20:35], v[116:119], v[60:63], v[20:35]
	v_exp_f32_e32 v115, v115
	v_exp_f32_e32 v36, v36
	v_exp_f32_e32 v37, v37
	s_waitcnt lgkmcnt(10)
	v_mfma_f32_32x32x16_f16 v[4:19], v[148:151], v[68:71], v[4:19]
	v_exp_f32_e32 v38, v38
	v_exp_f32_e32 v39, v39
	v_exp_f32_e32 v40, v40
	s_waitcnt lgkmcnt(8)
	v_mfma_f32_32x32x16_f16 v[20:35], v[148:151], v[64:67], v[20:35]
	v_exp_f32_e32 v41, v41
	v_exp_f32_e32 v42, v42
	v_exp_f32_e32 v43, v43
	s_waitcnt vmcnt(4) lgkmcnt(0)
	s_barrier
	ds_read_b64_tr_b16 v[166:167], v212 offset:16384
	ds_read_b64_tr_b16 v[168:169], v212 offset:16896
	s_waitcnt lgkmcnt(9)
	v_mfma_f32_32x32x16_bf16 v[68:83], v[92:95], v[140:143], -4.0
	v_cvt_pk_f16_f32 v124, v100, v101
	v_pk_add_f16 v0, v0, v150
	v_pk_add_f16 v52, v170, v151
	v_pk_add_f16 v0, v0, v52
	v_cvt_pk_f16_f32 v125, v102, v103
	v_dot2c_f32_f16_e32 v2, 0x3c003c00, v0
	ds_read_b64_tr_b16 v[92:93], v212 offset:20480
	ds_read_b64_tr_b16 v[94:95], v212 offset:20992
	s_waitcnt lgkmcnt(10)
	v_mfma_f32_32x32x16_bf16 v[52:67], v[96:99], v[140:143], -4.0
	v_exp_f32_e32 v44, v44
	v_cvt_pk_f16_f32 v126, v104, v105
	v_cvt_pk_f16_f32 v127, v106, v107
	ds_read_b64_tr_b16 v[96:97], v212 offset:17408
	ds_read_b64_tr_b16 v[98:99], v212 offset:17920
	s_waitcnt lgkmcnt(11)
	v_mfma_f32_32x32x16_bf16 v[68:83], v[144:147], v[128:131], v[68:83]
	v_exp_f32_e32 v45, v45
	v_cvt_pk_f16_f32 v120, v108, v109
	v_pk_add_f16 v0, v124, v126
	v_pk_add_f16 v104, v125, v127
	v_cvt_pk_f16_f32 v121, v110, v111
	ds_read_b64_tr_b16 v[100:101], v212 offset:21504
	ds_read_b64_tr_b16 v[102:103], v212 offset:22016
	s_waitcnt lgkmcnt(12)
	v_mfma_f32_32x32x16_bf16 v[52:67], v[152:155], v[128:131], v[52:67]
	v_exp_f32_e32 v46, v46
	v_exp_f32_e32 v47, v47
	v_pk_add_f16 v0, v0, v120
	v_pk_add_f16 v108, v104, v121
	v_cvt_pk_f16_f32 v122, v112, v113
	v_cvt_pk_f16_f32 v123, v114, v115
	ds_read_b64_tr_b16 v[104:105], v212 offset:18432
	ds_read_b64_tr_b16 v[106:107], v212 offset:18944
	s_waitcnt lgkmcnt(13)
	v_mfma_f32_32x32x16_bf16 v[68:83], v[156:159], v[136:139], v[68:83]
	v_exp_f32_e32 v48, v48
	v_exp_f32_e32 v49, v49
	v_cvt_pk_f16_f32 v116, v36, v37
	v_pk_add_f16 v0, v0, v122
	v_pk_add_f16 v108, v108, v123
	v_cvt_pk_f16_f32 v117, v38, v39
	ds_read_b64_tr_b16 v[36:37], v212 offset:22528
	ds_read_b64_tr_b16 v[38:39], v212 offset:23040
	s_waitcnt lgkmcnt(14)
	v_mfma_f32_32x32x16_bf16 v[52:67], v[160:163], v[136:139], v[52:67]
	v_exp_f32_e32 v50, v50
	v_pk_add_f16 v0, v0, v116
	v_pk_add_f16 v108, v108, v117
	v_cvt_pk_f16_f32 v118, v40, v41
	v_cvt_pk_f16_f32 v119, v42, v43
	ds_read_b64_tr_b16 v[40:41], v212 offset:19456
	ds_read_b64_tr_b16 v[42:43], v212 offset:19968
	s_waitcnt lgkmcnt(14)
	v_mfma_f32_32x32x16_bf16 v[68:83], v[88:91], v[132:135], v[68:83]
	v_exp_f32_e32 v51, v51
	v_cvt_pk_f16_f32 v148, v44, v45
	v_pk_add_f16 v0, v0, v118
	v_pk_add_f16 v88, v108, v119
	v_cvt_pk_f16_f32 v149, v46, v47
	ds_read_b64_tr_b16 v[44:45], v212 offset:23552
	ds_read_b64_tr_b16 v[46:47], v212 offset:24064
	v_mfma_f32_32x32x16_bf16 v[52:67], v[84:87], v[132:135], v[52:67]
	v_pk_add_f16 v0, v0, v148
	v_pk_add_f16 v170, v88, v149
	v_cvt_pk_f16_f32 v150, v48, v49
	v_cvt_pk_f16_f32 v151, v50, v51
	s_add_u32 s60, s56, 0x60000
	s_addc_u32 s61, s57, 0
	s_mov_b32 m0, s76
	s_nop 0
	global_load_lds_dwordx4 v165, s[60:61]
	s_add_u32 s60, s58, 0x48000
	s_addc_u32 s61, s59, 0
	s_mov_b32 m0, s10
	s_nop 0
	global_load_lds_dwordx4 v164, s[60:61]
	s_waitcnt lgkmcnt(14)
	v_mfma_f32_32x32x16_f16 v[4:19], v[124:127], v[166:169], v[4:19]
	v_exp_f32_e32 v68, v68
	v_exp_f32_e32 v69, v69
	v_exp_f32_e32 v70, v70
	s_waitcnt lgkmcnt(12)
	v_mfma_f32_32x32x16_f16 v[20:35], v[124:127], v[92:95], v[20:35]
	v_exp_f32_e32 v71, v71
	v_exp_f32_e32 v72, v72
	v_exp_f32_e32 v73, v73
	ds_read_b128 v[48:51], v210 offset:32768
	ds_read_b128 v[84:87], v210 offset:33280
	s_waitcnt lgkmcnt(12)
	v_mfma_f32_32x32x16_f16 v[4:19], v[120:123], v[96:99], v[4:19]
	v_exp_f32_e32 v74, v74
	v_exp_f32_e32 v75, v75
	v_exp_f32_e32 v76, v76
	ds_read_b128 v[88:91], v210 offset:34816
	ds_read_b128 v[92:95], v210 offset:35328
	s_waitcnt lgkmcnt(12)
	v_mfma_f32_32x32x16_f16 v[20:35], v[120:123], v[100:103], v[20:35]
	v_exp_f32_e32 v77, v77
	v_exp_f32_e32 v78, v78
	v_exp_f32_e32 v79, v79
	ds_read_b128 v[96:99], v210 offset:36864
	ds_read_b128 v[144:147], v210 offset:37376
	s_waitcnt lgkmcnt(12)
	v_mfma_f32_32x32x16_f16 v[4:19], v[116:119], v[104:107], v[4:19]
	v_exp_f32_e32 v80, v80
	v_exp_f32_e32 v81, v81
	v_exp_f32_e32 v82, v82
	ds_read_b128 v[152:155], v210 offset:38912
	ds_read_b128 v[156:159], v210 offset:39424
	s_waitcnt lgkmcnt(12)
	v_mfma_f32_32x32x16_f16 v[20:35], v[116:119], v[36:39], v[20:35]
	v_exp_f32_e32 v83, v83
	v_exp_f32_e32 v52, v52
	v_exp_f32_e32 v53, v53
	s_waitcnt lgkmcnt(10)
	v_mfma_f32_32x32x16_f16 v[4:19], v[148:151], v[40:43], v[4:19]
	v_exp_f32_e32 v54, v54
	v_exp_f32_e32 v55, v55
	v_exp_f32_e32 v56, v56
	s_waitcnt lgkmcnt(8)
	v_mfma_f32_32x32x16_f16 v[20:35], v[148:151], v[44:47], v[20:35]
	v_exp_f32_e32 v57, v57
	v_exp_f32_e32 v58, v58
	v_exp_f32_e32 v59, v59
	ds_read_b64_tr_b16 v[160:161], v212 offset:24576
	ds_read_b64_tr_b16 v[162:163], v212 offset:25088
	s_waitcnt lgkmcnt(9)
	v_mfma_f32_32x32x16_bf16 v[100:115], v[48:51], v[140:143], -4.0
	v_exp_f32_e32 v60, v60
	v_cvt_pk_f16_f32 v124, v68, v69
	v_pk_add_f16 v0, v0, v150
	v_pk_add_f16 v116, v170, v151
	v_cvt_pk_f16_f32 v125, v70, v71
	ds_read_b64_tr_b16 v[68:69], v212 offset:28672
	ds_read_b64_tr_b16 v[70:71], v212 offset:29184
	s_waitcnt lgkmcnt(10)
	v_mfma_f32_32x32x16_bf16 v[36:51], v[84:87], v[140:143], -4.0
	v_exp_f32_e32 v61, v61
	v_pk_add_f16 v0, v0, v124
	v_pk_add_f16 v84, v116, v125
	v_cvt_pk_f16_f32 v126, v72, v73
	v_cvt_pk_f16_f32 v127, v74, v75
	ds_read_b64_tr_b16 v[72:73], v212 offset:25600
	ds_read_b64_tr_b16 v[74:75], v212 offset:26112
	s_waitcnt lgkmcnt(11)
	v_mfma_f32_32x32x16_bf16 v[100:115], v[88:91], v[128:131], v[100:115]
	v_exp_f32_e32 v62, v62
	v_cvt_pk_f16_f32 v120, v76, v77
	v_pk_add_f16 v0, v0, v126
	v_pk_add_f16 v84, v84, v127
	v_cvt_pk_f16_f32 v121, v78, v79
	ds_read_b64_tr_b16 v[76:77], v212 offset:29696
	ds_read_b64_tr_b16 v[78:79], v212 offset:30208
	s_waitcnt lgkmcnt(12)
	v_mfma_f32_32x32x16_bf16 v[36:51], v[92:95], v[128:131], v[36:51]
	v_exp_f32_e32 v63, v63
	v_exp_f32_e32 v64, v64
	v_pk_add_f16 v0, v0, v120
	v_pk_add_f16 v84, v84, v121
	v_cvt_pk_f16_f32 v122, v80, v81
	v_cvt_pk_f16_f32 v123, v82, v83
	ds_read_b64_tr_b16 v[80:81], v212 offset:26624
	ds_read_b64_tr_b16 v[82:83], v212 offset:27136
	s_waitcnt lgkmcnt(13)
	v_mfma_f32_32x32x16_bf16 v[100:115], v[96:99], v[136:139], v[100:115]
	v_exp_f32_e32 v65, v65
	v_cvt_pk_f16_f32 v116, v52, v53
	v_pk_add_f16 v0, v0, v122
	v_pk_add_f16 v88, v84, v123
	v_cvt_pk_f16_f32 v117, v54, v55
	ds_read_b64_tr_b16 v[84:85], v212 offset:30720
	ds_read_b64_tr_b16 v[86:87], v212 offset:31232
	s_waitcnt lgkmcnt(14)
	v_mfma_f32_32x32x16_bf16 v[36:51], v[144:147], v[136:139], v[36:51]
	v_exp_f32_e32 v66, v66
	v_pk_add_f16 v0, v0, v116
	v_pk_add_f16 v52, v88, v117
	v_cvt_pk_f16_f32 v118, v56, v57
	v_cvt_pk_f16_f32 v119, v58, v59
	ds_read_b64_tr_b16 v[56:57], v212 offset:27648
	ds_read_b64_tr_b16 v[58:59], v212 offset:28160
	s_waitcnt lgkmcnt(14)
	v_mfma_f32_32x32x16_bf16 v[100:115], v[152:155], v[132:135], v[100:115]
	v_exp_f32_e32 v67, v67
	v_cvt_pk_f16_f32 v148, v60, v61
	v_pk_add_f16 v0, v0, v118
	v_pk_add_f16 v52, v52, v119
	v_cvt_pk_f16_f32 v149, v62, v63
	ds_read_b64_tr_b16 v[60:61], v212 offset:31744
	ds_read_b64_tr_b16 v[62:63], v212 offset:32256
	v_mfma_f32_32x32x16_bf16 v[36:51], v[156:159], v[132:135], v[36:51]
	v_pk_add_f16 v0, v0, v148
	v_pk_add_f16 v174, v52, v149
	v_cvt_pk_f16_f32 v150, v64, v65
	v_cvt_pk_f16_f32 v151, v66, v67
	s_add_u32 s60, s56, 0x6c000
	s_addc_u32 s61, s57, 0
	s_mov_b32 m0, s77
	s_nop 0
	global_load_lds_dwordx4 v165, s[60:61]
	s_add_u32 s60, s58, 0x54000
	s_addc_u32 s61, s59, 0
	s_mov_b32 m0, s78
	s_nop 0
	global_load_lds_dwordx4 v164, s[60:61]
	s_waitcnt lgkmcnt(14)
	v_mfma_f32_32x32x16_f16 v[4:19], v[124:127], v[160:163], v[4:19]
	v_exp_f32_e32 v100, v100
	v_exp_f32_e32 v101, v101
	v_exp_f32_e32 v102, v102
	s_waitcnt lgkmcnt(12)
	v_mfma_f32_32x32x16_f16 v[20:35], v[124:127], v[68:71], v[20:35]
	v_exp_f32_e32 v103, v103
	v_exp_f32_e32 v104, v104
	v_exp_f32_e32 v105, v105
	ds_read_b128 v[64:67], v210 offset:40960
	ds_read_b128 v[144:147], v210 offset:41472
	s_waitcnt lgkmcnt(12)
	v_mfma_f32_32x32x16_f16 v[4:19], v[120:123], v[72:75], v[4:19]
	v_exp_f32_e32 v106, v106
	v_exp_f32_e32 v107, v107
	v_exp_f32_e32 v108, v108
	ds_read_b128 v[152:155], v210 offset:43008
	ds_read_b128 v[156:159], v210 offset:43520
	s_waitcnt lgkmcnt(12)
	v_mfma_f32_32x32x16_f16 v[20:35], v[120:123], v[76:79], v[20:35]
	v_exp_f32_e32 v109, v109
	v_exp_f32_e32 v110, v110
	v_exp_f32_e32 v111, v111
	ds_read_b128 v[160:163], v210 offset:45056
	ds_read_b128 v[166:169], v210 offset:45568
	s_waitcnt lgkmcnt(12)
	v_mfma_f32_32x32x16_f16 v[4:19], v[116:119], v[80:83], v[4:19]
	v_exp_f32_e32 v112, v112
	v_exp_f32_e32 v113, v113
	v_exp_f32_e32 v114, v114
	ds_read_b128 v[170:173], v210 offset:47104
	ds_read_b128 v[52:55], v210 offset:47616
	s_waitcnt lgkmcnt(12)
	v_mfma_f32_32x32x16_f16 v[20:35], v[116:119], v[84:87], v[20:35]
	v_exp_f32_e32 v115, v115
	v_exp_f32_e32 v36, v36
	v_exp_f32_e32 v37, v37
	s_waitcnt lgkmcnt(10)
	v_mfma_f32_32x32x16_f16 v[4:19], v[148:151], v[56:59], v[4:19]
	v_exp_f32_e32 v38, v38
	v_exp_f32_e32 v39, v39
	v_exp_f32_e32 v40, v40
	s_waitcnt lgkmcnt(8)
	v_mfma_f32_32x32x16_f16 v[20:35], v[148:151], v[60:63], v[20:35]
	v_exp_f32_e32 v41, v41
	v_exp_f32_e32 v42, v42
	v_exp_f32_e32 v43, v43
	s_waitcnt vmcnt(4) lgkmcnt(0)
	s_barrier
	ds_read_b64_tr_b16 v[56:57], v212 offset:32768
	ds_read_b64_tr_b16 v[58:59], v212 offset:33280
	s_waitcnt lgkmcnt(9)
	v_mfma_f32_32x32x16_bf16 v[84:99], v[64:67], v[140:143], -4.0
	v_pk_add_f16 v0, v0, v150
	v_pk_add_f16 v60, v174, v151
	v_cvt_pk_f16_f32 v124, v100, v101
	v_pk_add_f16 v0, v0, v60
	v_cvt_pk_f16_f32 v125, v102, v103
	v_dot2c_f32_f16_e32 v2, 0x3c003c00, v0
	ds_read_b64_tr_b16 v[60:61], v212 offset:36864
	ds_read_b64_tr_b16 v[62:63], v212 offset:37376
	s_waitcnt lgkmcnt(10)
	v_mfma_f32_32x32x16_bf16 v[68:83], v[144:147], v[140:143], -4.0
	v_exp_f32_e32 v44, v44
	v_cvt_pk_f16_f32 v126, v104, v105
	v_cvt_pk_f16_f32 v127, v106, v107
	ds_read_b64_tr_b16 v[64:65], v212 offset:33792
	ds_read_b64_tr_b16 v[66:67], v212 offset:34304
	s_waitcnt lgkmcnt(11)
	v_mfma_f32_32x32x16_bf16 v[84:99], v[152:155], v[128:131], v[84:99]
	v_exp_f32_e32 v45, v45
	v_pk_add_f16 v0, v124, v126
	v_pk_add_f16 v104, v125, v127
	v_cvt_pk_f16_f32 v120, v108, v109
	v_cvt_pk_f16_f32 v121, v110, v111
	ds_read_b64_tr_b16 v[100:101], v212 offset:37888
	ds_read_b64_tr_b16 v[102:103], v212 offset:38400
	s_waitcnt lgkmcnt(12)
	v_mfma_f32_32x32x16_bf16 v[68:83], v[156:159], v[128:131], v[68:83]
	v_exp_f32_e32 v46, v46
	v_exp_f32_e32 v47, v47
	v_pk_add_f16 v0, v0, v120
	v_pk_add_f16 v108, v104, v121
	v_cvt_pk_f16_f32 v122, v112, v113
	v_cvt_pk_f16_f32 v123, v114, v115
	ds_read_b64_tr_b16 v[104:105], v212 offset:34816
	ds_read_b64_tr_b16 v[106:107], v212 offset:35328
	s_waitcnt lgkmcnt(13)
	v_mfma_f32_32x32x16_bf16 v[84:99], v[160:163], v[136:139], v[84:99]
	v_exp_f32_e32 v48, v48
	v_exp_f32_e32 v49, v49
	v_pk_add_f16 v0, v0, v122
	v_pk_add_f16 v108, v108, v123
	v_cvt_pk_f16_f32 v116, v36, v37
	v_cvt_pk_f16_f32 v117, v38, v39
	ds_read_b64_tr_b16 v[36:37], v212 offset:38912
	ds_read_b64_tr_b16 v[38:39], v212 offset:39424
	s_waitcnt lgkmcnt(14)
	v_mfma_f32_32x32x16_bf16 v[68:83], v[166:169], v[136:139], v[68:83]
	v_exp_f32_e32 v50, v50
	v_pk_add_f16 v0, v0, v116
	v_pk_add_f16 v108, v108, v117
	v_cvt_pk_f16_f32 v118, v40, v41
	v_cvt_pk_f16_f32 v119, v42, v43
	ds_read_b64_tr_b16 v[40:41], v212 offset:35840
	ds_read_b64_tr_b16 v[42:43], v212 offset:36352
	v_cvt_pk_f16_f32 v148, v44, v45
	v_pk_add_f16 v0, v0, v118
	v_pk_add_f16 v108, v108, v119
	v_cvt_pk_f16_f32 v149, v46, v47
	s_waitcnt lgkmcnt(14)
	v_mfma_f32_32x32x16_bf16 v[84:99], v[170:173], v[132:135], v[84:99]
	v_exp_f32_e32 v51, v51
	ds_read_b64_tr_b16 v[44:45], v212 offset:39936
	ds_read_b64_tr_b16 v[46:47], v212 offset:40448
	v_mfma_f32_32x32x16_bf16 v[68:83], v[52:55], v[132:135], v[68:83]
	v_pk_add_f16 v0, v0, v148
	v_pk_add_f16 v166, v108, v149
	v_cvt_pk_f16_f32 v150, v48, v49
	v_cvt_pk_f16_f32 v151, v50, v51
	s_add_u32 s60, s56, 0x78000
	s_addc_u32 s61, s57, 0
	s_mov_b32 m0, s79
	s_nop 0
	global_load_lds_dwordx4 v165, s[60:61]
	s_add_u32 s60, s58, 0x60000
	s_addc_u32 s61, s59, 0
	s_mov_b32 m0, s92
	s_nop 0
	global_load_lds_dwordx4 v164, s[60:61]
	s_waitcnt lgkmcnt(14)
	v_mfma_f32_32x32x16_f16 v[4:19], v[124:127], v[56:59], v[4:19]
	v_exp_f32_e32 v84, v84
	v_exp_f32_e32 v85, v85
	v_exp_f32_e32 v86, v86
	s_waitcnt lgkmcnt(12)
	v_mfma_f32_32x32x16_f16 v[20:35], v[124:127], v[60:63], v[20:35]
	v_exp_f32_e32 v87, v87
	v_exp_f32_e32 v88, v88
	v_exp_f32_e32 v89, v89
	ds_read_b128 v[48:51], v210
	ds_read_b128 v[108:111], v210 offset:512
	s_waitcnt lgkmcnt(12)
	v_mfma_f32_32x32x16_f16 v[4:19], v[120:123], v[64:67], v[4:19]
	v_exp_f32_e32 v90, v90
	v_exp_f32_e32 v91, v91
	v_exp_f32_e32 v92, v92
	ds_read_b128 v[112:115], v210 offset:2048
	ds_read_b128 v[144:147], v210 offset:2560
	s_waitcnt lgkmcnt(12)
	v_mfma_f32_32x32x16_f16 v[20:35], v[120:123], v[100:103], v[20:35]
	v_exp_f32_e32 v93, v93
	v_exp_f32_e32 v94, v94
	v_exp_f32_e32 v95, v95
	ds_read_b128 v[100:103], v210 offset:4096
	ds_read_b128 v[152:155], v210 offset:4608
	s_waitcnt lgkmcnt(12)
	v_mfma_f32_32x32x16_f16 v[4:19], v[116:119], v[104:107], v[4:19]
	v_exp_f32_e32 v96, v96
	v_exp_f32_e32 v97, v97
	v_exp_f32_e32 v98, v98
	ds_read_b128 v[104:107], v210 offset:6144
	ds_read_b128 v[156:159], v210 offset:6656
	s_waitcnt lgkmcnt(12)
	v_mfma_f32_32x32x16_f16 v[20:35], v[116:119], v[36:39], v[20:35]
	v_exp_f32_e32 v99, v99
	v_exp_f32_e32 v68, v68
	v_exp_f32_e32 v69, v69
	s_waitcnt lgkmcnt(10)
	v_mfma_f32_32x32x16_f16 v[4:19], v[148:151], v[40:43], v[4:19]
	v_exp_f32_e32 v70, v70
	v_exp_f32_e32 v71, v71
	v_exp_f32_e32 v72, v72
	s_waitcnt lgkmcnt(8)
	v_mfma_f32_32x32x16_f16 v[20:35], v[148:151], v[44:47], v[20:35]
	v_exp_f32_e32 v73, v73
	v_exp_f32_e32 v74, v74
	v_exp_f32_e32 v75, v75
	ds_read_b64_tr_b16 v[160:161], v212 offset:40960
	ds_read_b64_tr_b16 v[162:163], v212 offset:41472
	s_waitcnt lgkmcnt(9)
	v_mfma_f32_32x32x16_bf16 v[52:67], v[48:51], v[140:143], -4.0
	v_exp_f32_e32 v76, v76
	v_cvt_pk_f16_f32 v124, v84, v85
	v_pk_add_f16 v0, v0, v150
	v_pk_add_f16 v116, v166, v151
	v_cvt_pk_f16_f32 v125, v86, v87
	ds_read_b64_tr_b16 v[84:85], v212 offset:45056
	ds_read_b64_tr_b16 v[86:87], v212 offset:45568
	s_waitcnt lgkmcnt(10)
	v_mfma_f32_32x32x16_bf16 v[36:51], v[108:111], v[140:143], -4.0
	v_exp_f32_e32 v77, v77
	v_pk_add_f16 v0, v0, v124
	v_pk_add_f16 v108, v116, v125
	v_cvt_pk_f16_f32 v126, v88, v89
	v_cvt_pk_f16_f32 v127, v90, v91
	ds_read_b64_tr_b16 v[88:89], v212 offset:41984
	ds_read_b64_tr_b16 v[90:91], v212 offset:42496
	s_waitcnt lgkmcnt(11)
	v_mfma_f32_32x32x16_bf16 v[52:67], v[112:115], v[128:131], v[52:67]
	v_exp_f32_e32 v78, v78
	v_cvt_pk_f16_f32 v120, v92, v93
	v_pk_add_f16 v0, v0, v126
	v_pk_add_f16 v108, v108, v127
	v_cvt_pk_f16_f32 v121, v94, v95
	ds_read_b64_tr_b16 v[92:93], v212 offset:46080
	ds_read_b64_tr_b16 v[94:95], v212 offset:46592
	s_waitcnt lgkmcnt(12)
	v_mfma_f32_32x32x16_bf16 v[36:51], v[144:147], v[128:131], v[36:51]
	v_exp_f32_e32 v79, v79
	v_exp_f32_e32 v80, v80
	v_pk_add_f16 v0, v0, v120
	v_pk_add_f16 v108, v108, v121
	v_cvt_pk_f16_f32 v122, v96, v97
	v_cvt_pk_f16_f32 v123, v98, v99
	ds_read_b64_tr_b16 v[96:97], v212 offset:43008
	ds_read_b64_tr_b16 v[98:99], v212 offset:43520
	s_waitcnt lgkmcnt(13)
	v_mfma_f32_32x32x16_bf16 v[52:67], v[100:103], v[136:139], v[52:67]
	v_exp_f32_e32 v81, v81
	v_cvt_pk_f16_f32 v116, v68, v69
	v_pk_add_f16 v0, v0, v122
	v_pk_add_f16 v100, v108, v123
	v_cvt_pk_f16_f32 v117, v70, v71
	ds_read_b64_tr_b16 v[166:167], v212 offset:47104
	ds_read_b64_tr_b16 v[168:169], v212 offset:47616
	s_waitcnt lgkmcnt(14)
	v_mfma_f32_32x32x16_bf16 v[36:51], v[152:155], v[136:139], v[36:51]
	v_exp_f32_e32 v82, v82
	v_pk_add_f16 v0, v0, v116
	v_pk_add_f16 v68, v100, v117
	v_cvt_pk_f16_f32 v118, v72, v73
	v_cvt_pk_f16_f32 v119, v74, v75
	ds_read_b64_tr_b16 v[170:171], v212 offset:44032
	ds_read_b64_tr_b16 v[172:173], v212 offset:44544
	s_waitcnt lgkmcnt(14)
	v_mfma_f32_32x32x16_bf16 v[52:67], v[104:107], v[132:135], v[52:67]
	v_exp_f32_e32 v83, v83
	v_cvt_pk_f16_f32 v148, v76, v77
	v_pk_add_f16 v0, v0, v118
	v_pk_add_f16 v68, v68, v119
	v_cvt_pk_f16_f32 v149, v78, v79
	ds_read_b64_tr_b16 v[74:75], v212 offset:48128
	ds_read_b64_tr_b16 v[76:77], v212 offset:48640
	v_mfma_f32_32x32x16_bf16 v[36:51], v[156:159], v[132:135], v[36:51]
	v_cvt_pk_f16_f32 v150, v80, v81
	v_mov_b64_e32 v[144:145], v[148:149]
	v_pk_add_f16 v72, v0, v148
	v_cvt_pk_f16_f32 v0, v82, v83
	v_mov_b64_e32 v[146:147], v[150:151]
	v_pk_add_f16 v73, v68, v149
	v_mov_b32_e32 v147, v0
	s_add_u32 s56, s56, 0x84000
	s_addc_u32 s57, s57, 0
	s_mov_b32 m0, s85
	s_nop 0
	global_load_lds_dwordx4 v165, s[56:57]
	s_add_u32 s56, s58, 0x6c000
	s_addc_u32 s57, s59, 0
	s_mov_b32 m0, s93
	s_nop 0
	global_load_lds_dwordx4 v164, s[56:57]
	s_waitcnt lgkmcnt(14)
	v_mfma_f32_32x32x16_f16 v[4:19], v[124:127], v[160:163], v[4:19]
	v_exp_f32_e32 v52, v52
	v_exp_f32_e32 v53, v53
	v_exp_f32_e32 v54, v54
	s_waitcnt lgkmcnt(12)
	v_mfma_f32_32x32x16_f16 v[20:35], v[124:127], v[84:87], v[20:35]
	v_exp_f32_e32 v55, v55
	v_exp_f32_e32 v56, v56
	v_exp_f32_e32 v57, v57
	ds_read_b128 v[68:71], v210 offset:8192
	ds_read_b128 v[160:163], v210 offset:8704
	s_waitcnt lgkmcnt(12)
	v_mfma_f32_32x32x16_f16 v[4:19], v[120:123], v[88:91], v[4:19]
	v_exp_f32_e32 v58, v58
	v_exp_f32_e32 v59, v59
	v_exp_f32_e32 v60, v60
	ds_read_b128 v[156:159], v210 offset:10240
	ds_read_b128 v[112:115], v210 offset:10752
	s_waitcnt lgkmcnt(12)
	v_mfma_f32_32x32x16_f16 v[20:35], v[120:123], v[92:95], v[20:35]
	v_exp_f32_e32 v61, v61
	v_exp_f32_e32 v62, v62
	v_exp_f32_e32 v63, v63
	ds_read_b128 v[152:155], v210 offset:12288
	ds_read_b128 v[104:107], v210 offset:12800
	s_waitcnt lgkmcnt(12)
	v_mfma_f32_32x32x16_f16 v[4:19], v[116:119], v[96:99], v[4:19]
	v_exp_f32_e32 v64, v64
	v_exp_f32_e32 v65, v65
	v_exp_f32_e32 v66, v66
	ds_read_b128 v[108:111], v210 offset:14336
	ds_read_b128 v[100:103], v210 offset:14848
	s_waitcnt lgkmcnt(12)
	v_mfma_f32_32x32x16_f16 v[20:35], v[116:119], v[166:169], v[20:35]
	v_exp_f32_e32 v67, v67
	v_exp_f32_e32 v36, v36
	v_exp_f32_e32 v37, v37
	s_waitcnt lgkmcnt(10)
	v_mfma_f32_32x32x16_f16 v[4:19], v[144:147], v[170:173], v[4:19]
	v_exp_f32_e32 v38, v38
	v_exp_f32_e32 v39, v39
	v_exp_f32_e32 v40, v40
	s_waitcnt lgkmcnt(8)
	v_mfma_f32_32x32x16_f16 v[20:35], v[144:147], v[74:77], v[20:35]
	v_exp_f32_e32 v41, v41
	v_exp_f32_e32 v42, v42
	v_exp_f32_e32 v43, v43
	s_add_i32 s53, s53, 6
	s_add_u32 s54, s54, 0x48000
	s_addc_u32 s55, s55, 0
	v_mov_b32_e32 v151, v0
	s_cmpk_gt_u32 s53, 0xef
	s_waitcnt vmcnt(4) lgkmcnt(0)
	s_barrier
	s_cbranch_scc0 .LBB0_336
	v_exp_f32_e32 v44, v44
	v_exp_f32_e32 v45, v45
	v_exp_f32_e32 v46, v46
	v_exp_f32_e32 v47, v47
	v_exp_f32_e32 v48, v48
	v_exp_f32_e32 v49, v49
	v_exp_f32_e32 v50, v50
	v_exp_f32_e32 v51, v51
	s_and_b32 s11, s11, 0x3fffffc0
	s_lshl_b32 s11, s11, 2
	s_add_i32 s11, s11, 0
	s_add_i32 s11, s11, 0x18000
	ds_read_b64_tr_b16 v[148:149], v211 offset:49152
	ds_read_b64_tr_b16 v[150:151], v211 offset:49664
	s_waitcnt lgkmcnt(9)
	v_mfma_f32_32x32x16_bf16 v[84:99], v[68:71], v[140:143], -4.0
	v_mov_b32_e32 v116, v3
	v_pk_add_f16 v0, v72, v146
	v_pk_add_f16 v68, v73, v147
	v_cvt_pk_f16_f32 v124, v52, v53
	v_pk_add_f16 v0, v0, v68
	v_cvt_pk_f16_f32 v125, v54, v55
	v_dot2c_f32_f16_e32 v2, 0x3c003c00, v0
	v_mov_b32_e32 v0, v3
	ds_read_b64_tr_b16 v[52:53], v211 offset:53248
	ds_read_b64_tr_b16 v[54:55], v211 offset:53760
	s_waitcnt lgkmcnt(10)
	v_mfma_f32_32x32x16_bf16 v[68:83], v[160:163], v[140:143], -4.0
	s_nop 0
	v_pk_add_f16 v0, v0, v124
	v_pk_add_f16 v116, v116, v125
	v_cvt_pk_f16_f32 v126, v56, v57
	v_cvt_pk_f16_f32 v127, v58, v59
	ds_read_b64_tr_b16 v[56:57], v211 offset:50176
	ds_read_b64_tr_b16 v[58:59], v211 offset:50688
	s_waitcnt lgkmcnt(11)
	v_mfma_f32_32x32x16_bf16 v[84:99], v[156:159], v[128:131], v[84:99]
	v_pk_add_f16 v0, v0, v126
	v_pk_add_f16 v116, v116, v127
	v_cvt_pk_f16_f32 v120, v60, v61
	v_cvt_pk_f16_f32 v121, v62, v63
	ds_read_b64_tr_b16 v[60:61], v211 offset:54272
	ds_read_b64_tr_b16 v[62:63], v211 offset:54784
	s_waitcnt lgkmcnt(12)
	v_mfma_f32_32x32x16_bf16 v[68:83], v[112:115], v[128:131], v[68:83]
	v_pk_add_f16 v0, v0, v120
	v_pk_add_f16 v116, v116, v121
	v_cvt_pk_f16_f32 v122, v64, v65
	v_cvt_pk_f16_f32 v123, v66, v67
	ds_read_b64_tr_b16 v[64:65], v211 offset:51200
	ds_read_b64_tr_b16 v[66:67], v211 offset:51712
	s_waitcnt lgkmcnt(13)
	v_mfma_f32_32x32x16_bf16 v[84:99], v[152:155], v[136:139], v[84:99]
	v_pk_add_f16 v0, v0, v122
	v_pk_add_f16 v112, v116, v123
	v_cvt_pk_f16_f32 v116, v36, v37
	v_cvt_pk_f16_f32 v117, v38, v39
	ds_read_b64_tr_b16 v[36:37], v211 offset:55296
	ds_read_b64_tr_b16 v[38:39], v211 offset:55808
	s_waitcnt lgkmcnt(14)
	v_mfma_f32_32x32x16_bf16 v[68:83], v[104:107], v[136:139], v[68:83]
	v_pk_add_f16 v0, v0, v116
	v_pk_add_f16 v112, v112, v117
	v_cvt_pk_f16_f32 v118, v40, v41
	v_cvt_pk_f16_f32 v119, v42, v43
	ds_read_b64_tr_b16 v[40:41], v211 offset:52224
	ds_read_b64_tr_b16 v[42:43], v211 offset:52736
	s_waitcnt lgkmcnt(14)
	v_mfma_f32_32x32x16_bf16 v[84:99], v[108:111], v[132:135], v[84:99]
	v_pk_add_f16 v0, v0, v118
	v_pk_add_f16 v104, v112, v119
	v_cvt_pk_f16_f32 v144, v44, v45
	v_cvt_pk_f16_f32 v145, v46, v47
	ds_read_b64_tr_b16 v[44:45], v211 offset:56320
	ds_read_b64_tr_b16 v[46:47], v211 offset:56832
	v_mfma_f32_32x32x16_bf16 v[68:83], v[100:103], v[132:135], v[68:83]
	v_pk_add_f16 v0, v0, v144
	v_pk_add_f16 v166, v104, v145
	v_cvt_pk_f16_f32 v146, v48, v49
	v_cvt_pk_f16_f32 v147, v50, v51
	s_add_u32 s54, s88, 0xbd0000
	s_addc_u32 s55, s89, 0
	s_mov_b32 m0, s70
	s_nop 0
	global_load_lds_dwordx4 v165, s[54:55]
	s_add_u32 s54, s14, 0xbb8000
	s_addc_u32 s55, s15, 0
	s_cmp_lg_u32 0, -1
	s_cselect_b32 s53, 0, 0
	s_add_i32 s44, s53, s44
	s_add_i32 s53, s44, 0x14000
	s_mov_b32 m0, s53
	s_nop 0
	global_load_lds_dwordx4 v164, s[54:55]
	s_waitcnt lgkmcnt(14)
	v_mfma_f32_32x32x16_f16 v[4:19], v[124:127], v[148:151], v[4:19]
	v_exp_f32_e32 v84, v84
	v_exp_f32_e32 v85, v85
	v_exp_f32_e32 v86, v86
	v_exp_f32_e32 v87, v87
	s_waitcnt lgkmcnt(12)
	v_mfma_f32_32x32x16_f16 v[20:35], v[124:127], v[52:55], v[20:35]
	v_exp_f32_e32 v88, v88
	v_exp_f32_e32 v89, v89
	v_exp_f32_e32 v90, v90
	v_exp_f32_e32 v91, v91
	ds_read_b128 v[48:51], v210 offset:16384
	ds_read_b128 v[52:55], v210 offset:16896
	s_waitcnt lgkmcnt(12)
	v_mfma_f32_32x32x16_f16 v[4:19], v[120:123], v[56:59], v[4:19]
	v_exp_f32_e32 v92, v92
	v_exp_f32_e32 v93, v93
	v_exp_f32_e32 v94, v94
	v_exp_f32_e32 v95, v95
	ds_read_b128 v[56:59], v210 offset:18432
	ds_read_b128 v[148:151], v210 offset:18944
	s_waitcnt lgkmcnt(12)
	v_mfma_f32_32x32x16_f16 v[20:35], v[120:123], v[60:63], v[20:35]
	v_exp_f32_e32 v96, v96
	v_exp_f32_e32 v97, v97
	v_exp_f32_e32 v98, v98
	v_exp_f32_e32 v99, v99
	ds_read_b128 v[60:63], v210 offset:20480
	ds_read_b128 v[152:155], v210 offset:20992
	s_waitcnt lgkmcnt(12)
	v_mfma_f32_32x32x16_f16 v[4:19], v[116:119], v[64:67], v[4:19]
	v_exp_f32_e32 v68, v68
	v_exp_f32_e32 v69, v69
	v_exp_f32_e32 v70, v70
	v_exp_f32_e32 v71, v71
	ds_read_b128 v[64:67], v210 offset:22528
	ds_read_b128 v[156:159], v210 offset:23040
	s_waitcnt lgkmcnt(12)
	v_mfma_f32_32x32x16_f16 v[20:35], v[116:119], v[36:39], v[20:35]
	v_exp_f32_e32 v72, v72
	v_exp_f32_e32 v73, v73
	v_exp_f32_e32 v74, v74
	v_exp_f32_e32 v75, v75
	s_waitcnt lgkmcnt(10)
	v_mfma_f32_32x32x16_f16 v[4:19], v[144:147], v[40:43], v[4:19]
	v_exp_f32_e32 v76, v76
	v_exp_f32_e32 v77, v77
	v_exp_f32_e32 v78, v78
	v_exp_f32_e32 v79, v79
	s_waitcnt lgkmcnt(8)
	v_mfma_f32_32x32x16_f16 v[20:35], v[144:147], v[44:47], v[20:35]
	v_exp_f32_e32 v80, v80
	v_exp_f32_e32 v81, v81
	v_exp_f32_e32 v82, v82
	v_exp_f32_e32 v83, v83
	ds_read_b64_tr_b16 v[160:161], v211 offset:57344
	ds_read_b64_tr_b16 v[162:163], v211 offset:57856
	s_waitcnt lgkmcnt(9)
	v_mfma_f32_32x32x16_bf16 v[100:115], v[48:51], v[140:143], -4.0
	v_cvt_pk_f16_f32 v124, v84, v85
	v_pk_add_f16 v0, v0, v146
	v_pk_add_f16 v116, v166, v147
	v_cvt_pk_f16_f32 v125, v86, v87
	ds_read_b64_tr_b16 v[84:85], v211 offset:61440
	ds_read_b64_tr_b16 v[86:87], v211 offset:61952
	s_waitcnt lgkmcnt(10)
	v_mfma_f32_32x32x16_bf16 v[36:51], v[52:55], v[140:143], -4.0
	s_nop 0
	v_pk_add_f16 v0, v0, v124
	v_pk_add_f16 v116, v116, v125
	v_cvt_pk_f16_f32 v126, v88, v89
	v_cvt_pk_f16_f32 v127, v90, v91
	ds_read_b64_tr_b16 v[52:53], v211 offset:58368
	ds_read_b64_tr_b16 v[54:55], v211 offset:58880
	s_waitcnt lgkmcnt(11)
	v_mfma_f32_32x32x16_bf16 v[100:115], v[56:59], v[128:131], v[100:115]
	v_pk_add_f16 v0, v0, v126
	v_pk_add_f16 v88, v116, v127
	v_cvt_pk_f16_f32 v120, v92, v93
	v_cvt_pk_f16_f32 v121, v94, v95
	ds_read_b64_tr_b16 v[56:57], v211 offset:62464
	ds_read_b64_tr_b16 v[58:59], v211 offset:62976
	s_waitcnt lgkmcnt(12)
	v_mfma_f32_32x32x16_bf16 v[36:51], v[148:151], v[128:131], v[36:51]
	s_nop 0
	v_pk_add_f16 v0, v0, v120
	v_pk_add_f16 v92, v88, v121
	v_cvt_pk_f16_f32 v122, v96, v97
	v_cvt_pk_f16_f32 v123, v98, v99
	ds_read_b64_tr_b16 v[88:89], v211 offset:59392
	ds_read_b64_tr_b16 v[90:91], v211 offset:59904
	s_waitcnt lgkmcnt(13)
	v_mfma_f32_32x32x16_bf16 v[100:115], v[60:63], v[136:139], v[100:115]
	v_pk_add_f16 v0, v0, v122
	v_pk_add_f16 v92, v92, v123
	v_cvt_pk_f16_f32 v116, v68, v69
	v_cvt_pk_f16_f32 v117, v70, v71
	ds_read_b64_tr_b16 v[60:61], v211 offset:63488
	ds_read_b64_tr_b16 v[62:63], v211 offset:64000
	s_waitcnt lgkmcnt(14)
	v_mfma_f32_32x32x16_bf16 v[36:51], v[152:155], v[136:139], v[36:51]
	s_nop 0
	v_pk_add_f16 v0, v0, v116
	v_pk_add_f16 v68, v92, v117
	v_cvt_pk_f16_f32 v118, v72, v73
	v_cvt_pk_f16_f32 v119, v74, v75
	ds_read_b64_tr_b16 v[72:73], v211 offset:60416
	ds_read_b64_tr_b16 v[74:75], v211 offset:60928
	s_waitcnt lgkmcnt(14)
	v_mfma_f32_32x32x16_bf16 v[100:115], v[64:67], v[132:135], v[100:115]
	v_pk_add_f16 v0, v0, v118
	v_pk_add_f16 v68, v68, v119
	v_cvt_pk_f16_f32 v144, v76, v77
	v_cvt_pk_f16_f32 v145, v78, v79
	ds_read_b64_tr_b16 v[64:65], v211 offset:64512
	ds_read_b64_tr_b16 v[66:67], v211 offset:65024
	v_mfma_f32_32x32x16_bf16 v[36:51], v[156:159], v[132:135], v[36:51]
	s_nop 0
	v_pk_add_f16 v0, v0, v144
	v_pk_add_f16 v170, v68, v145
	v_cvt_pk_f16_f32 v146, v80, v81
	v_cvt_pk_f16_f32 v147, v82, v83
	s_add_u32 s54, s88, 0xbdc000
	s_addc_u32 s55, s89, 0
	s_add_i32 s53, s44, 0x2000
	s_mov_b32 m0, s53
	s_nop 0
	global_load_lds_dwordx4 v165, s[54:55]
	s_add_u32 s54, s14, 0xbc4000
	s_addc_u32 s55, s15, 0
	s_add_i32 s53, s44, 0x16000
	s_mov_b32 m0, s53
	s_nop 0
	global_load_lds_dwordx4 v164, s[54:55]
	s_waitcnt lgkmcnt(14)
	v_mfma_f32_32x32x16_f16 v[4:19], v[124:127], v[160:163], v[4:19]
	v_exp_f32_e32 v100, v100
	v_exp_f32_e32 v101, v101
	v_exp_f32_e32 v102, v102
	v_exp_f32_e32 v103, v103
	s_waitcnt lgkmcnt(12)
	v_mfma_f32_32x32x16_f16 v[20:35], v[124:127], v[84:87], v[20:35]
	v_exp_f32_e32 v104, v104
	v_exp_f32_e32 v105, v105
	v_exp_f32_e32 v106, v106
	v_exp_f32_e32 v107, v107
	ds_read_b128 v[76:79], v210 offset:24576
	ds_read_b128 v[80:83], v210 offset:25088
	s_waitcnt lgkmcnt(12)
	v_mfma_f32_32x32x16_f16 v[4:19], v[120:123], v[52:55], v[4:19]
	v_exp_f32_e32 v108, v108
	v_exp_f32_e32 v109, v109
	v_exp_f32_e32 v110, v110
	v_exp_f32_e32 v111, v111
	ds_read_b128 v[148:151], v210 offset:26624
	ds_read_b128 v[152:155], v210 offset:27136
	s_waitcnt lgkmcnt(12)
	v_mfma_f32_32x32x16_f16 v[20:35], v[120:123], v[56:59], v[20:35]
	v_exp_f32_e32 v112, v112
	v_exp_f32_e32 v113, v113
	v_exp_f32_e32 v114, v114
	v_exp_f32_e32 v115, v115
	ds_read_b128 v[156:159], v210 offset:28672
	ds_read_b128 v[160:163], v210 offset:29184
	s_waitcnt lgkmcnt(12)
	v_mfma_f32_32x32x16_f16 v[4:19], v[116:119], v[88:91], v[4:19]
	v_exp_f32_e32 v36, v36
	v_exp_f32_e32 v37, v37
	v_exp_f32_e32 v38, v38
	v_exp_f32_e32 v39, v39
	ds_read_b128 v[166:169], v210 offset:30720
	ds_read_b128 v[68:71], v210 offset:31232
	s_waitcnt lgkmcnt(12)
	v_mfma_f32_32x32x16_f16 v[20:35], v[116:119], v[60:63], v[20:35]
	v_exp_f32_e32 v40, v40
	v_exp_f32_e32 v41, v41
	v_exp_f32_e32 v42, v42
	v_exp_f32_e32 v43, v43
	s_waitcnt lgkmcnt(10)
	v_mfma_f32_32x32x16_f16 v[4:19], v[144:147], v[72:75], v[4:19]
	v_exp_f32_e32 v44, v44
	v_exp_f32_e32 v45, v45
	v_exp_f32_e32 v46, v46
	v_exp_f32_e32 v47, v47
	s_waitcnt lgkmcnt(8)
	v_mfma_f32_32x32x16_f16 v[20:35], v[144:147], v[64:67], v[20:35]
	v_exp_f32_e32 v48, v48
	v_exp_f32_e32 v49, v49
	v_exp_f32_e32 v50, v50
	v_exp_f32_e32 v51, v51
	s_waitcnt vmcnt(4) lgkmcnt(0)
	s_barrier
	ds_read_b64_tr_b16 v[72:73], v212 offset:16384
	ds_read_b64_tr_b16 v[74:75], v212 offset:16896
	s_waitcnt lgkmcnt(9)
	v_mfma_f32_32x32x16_bf16 v[84:99], v[76:79], v[140:143], -4.0
	v_cvt_pk_f16_f32 v124, v100, v101
	v_pk_add_f16 v0, v0, v146
	v_pk_add_f16 v52, v170, v147
	v_mov_b32_e32 v100, v3
	v_pk_add_f16 v0, v0, v52
	v_cvt_pk_f16_f32 v125, v102, v103
	v_dot2c_f32_f16_e32 v2, 0x3c003c00, v0
	v_mov_b32_e32 v0, v3
	ds_read_b64_tr_b16 v[76:77], v212 offset:20480
	ds_read_b64_tr_b16 v[78:79], v212 offset:20992
	s_waitcnt lgkmcnt(10)
	v_mfma_f32_32x32x16_bf16 v[52:67], v[80:83], v[140:143], -4.0
	s_nop 0
	v_pk_add_f16 v0, v0, v124
	v_pk_add_f16 v100, v100, v125
	v_cvt_pk_f16_f32 v126, v104, v105
	v_cvt_pk_f16_f32 v127, v106, v107
	ds_read_b64_tr_b16 v[80:81], v212 offset:17408
	ds_read_b64_tr_b16 v[82:83], v212 offset:17920
	s_waitcnt lgkmcnt(11)
	v_mfma_f32_32x32x16_bf16 v[84:99], v[148:151], v[128:131], v[84:99]
	v_pk_add_f16 v0, v0, v126
	v_pk_add_f16 v104, v100, v127
	v_cvt_pk_f16_f32 v120, v108, v109
	v_cvt_pk_f16_f32 v121, v110, v111
	ds_read_b64_tr_b16 v[100:101], v212 offset:21504
	ds_read_b64_tr_b16 v[102:103], v212 offset:22016
	s_waitcnt lgkmcnt(12)
	v_mfma_f32_32x32x16_bf16 v[52:67], v[152:155], v[128:131], v[52:67]
	v_pk_add_f16 v0, v0, v120
	v_pk_add_f16 v108, v104, v121
	v_cvt_pk_f16_f32 v122, v112, v113
	v_cvt_pk_f16_f32 v123, v114, v115
	ds_read_b64_tr_b16 v[104:105], v212 offset:18432
	ds_read_b64_tr_b16 v[106:107], v212 offset:18944
	s_waitcnt lgkmcnt(13)
	v_mfma_f32_32x32x16_bf16 v[84:99], v[156:159], v[136:139], v[84:99]
	v_pk_add_f16 v0, v0, v122
	v_pk_add_f16 v108, v108, v123
	v_cvt_pk_f16_f32 v116, v36, v37
	v_cvt_pk_f16_f32 v117, v38, v39
	ds_read_b64_tr_b16 v[36:37], v212 offset:22528
	ds_read_b64_tr_b16 v[38:39], v212 offset:23040
	s_waitcnt lgkmcnt(14)
	v_mfma_f32_32x32x16_bf16 v[52:67], v[160:163], v[136:139], v[52:67]
	v_pk_add_f16 v0, v0, v116
	v_pk_add_f16 v108, v108, v117
	v_cvt_pk_f16_f32 v118, v40, v41
	v_cvt_pk_f16_f32 v119, v42, v43
	ds_read_b64_tr_b16 v[40:41], v212 offset:19456
	ds_read_b64_tr_b16 v[42:43], v212 offset:19968
	s_waitcnt lgkmcnt(14)
	v_mfma_f32_32x32x16_bf16 v[84:99], v[166:169], v[132:135], v[84:99]
	v_pk_add_f16 v0, v0, v118
	v_pk_add_f16 v108, v108, v119
	v_cvt_pk_f16_f32 v144, v44, v45
	v_cvt_pk_f16_f32 v145, v46, v47
	ds_read_b64_tr_b16 v[44:45], v212 offset:23552
	ds_read_b64_tr_b16 v[46:47], v212 offset:24064
	v_mfma_f32_32x32x16_bf16 v[52:67], v[68:71], v[132:135], v[52:67]
	v_pk_add_f16 v0, v0, v144
	v_pk_add_f16 v166, v108, v145
	v_cvt_pk_f16_f32 v146, v48, v49
	v_cvt_pk_f16_f32 v147, v50, v51
	s_add_u32 s54, s88, 0xbe8000
	s_addc_u32 s55, s89, 0
	s_add_i32 s53, s44, 0x4000
	s_mov_b32 m0, s53
	s_nop 0
	global_load_lds_dwordx4 v165, s[54:55]
	s_add_u32 s54, s14, 0xbd0000
	s_addc_u32 s55, s15, 0
	s_mov_b32 m0, s10
	s_nop 0
	global_load_lds_dwordx4 v164, s[54:55]
	s_waitcnt lgkmcnt(14)
	v_mfma_f32_32x32x16_f16 v[4:19], v[124:127], v[72:75], v[4:19]
	v_exp_f32_e32 v84, v84
	v_exp_f32_e32 v85, v85
	v_exp_f32_e32 v86, v86
	v_exp_f32_e32 v87, v87
	s_waitcnt lgkmcnt(12)
	v_mfma_f32_32x32x16_f16 v[20:35], v[124:127], v[76:79], v[20:35]
	v_exp_f32_e32 v88, v88
	v_exp_f32_e32 v89, v89
	v_exp_f32_e32 v90, v90
	v_exp_f32_e32 v91, v91
	ds_read_b128 v[48:51], v210 offset:32768
	ds_read_b128 v[108:111], v210 offset:33280
	s_waitcnt lgkmcnt(12)
	v_mfma_f32_32x32x16_f16 v[4:19], v[120:123], v[80:83], v[4:19]
	v_exp_f32_e32 v92, v92
	v_exp_f32_e32 v93, v93
	v_exp_f32_e32 v94, v94
	v_exp_f32_e32 v95, v95
	ds_read_b128 v[112:115], v210 offset:34816
	ds_read_b128 v[148:151], v210 offset:35328
	s_waitcnt lgkmcnt(12)
	v_mfma_f32_32x32x16_f16 v[20:35], v[120:123], v[100:103], v[20:35]
	v_exp_f32_e32 v96, v96
	v_exp_f32_e32 v97, v97
	v_exp_f32_e32 v98, v98
	v_exp_f32_e32 v99, v99
	ds_read_b128 v[100:103], v210 offset:36864
	ds_read_b128 v[152:155], v210 offset:37376
	s_waitcnt lgkmcnt(12)
	v_mfma_f32_32x32x16_f16 v[4:19], v[116:119], v[104:107], v[4:19]
	v_exp_f32_e32 v52, v52
	v_exp_f32_e32 v53, v53
	v_exp_f32_e32 v54, v54
	v_exp_f32_e32 v55, v55
	ds_read_b128 v[104:107], v210 offset:38912
	ds_read_b128 v[156:159], v210 offset:39424
	s_waitcnt lgkmcnt(12)
	v_mfma_f32_32x32x16_f16 v[20:35], v[116:119], v[36:39], v[20:35]
	v_exp_f32_e32 v56, v56
	v_exp_f32_e32 v57, v57
	v_exp_f32_e32 v58, v58
	v_exp_f32_e32 v59, v59
	s_waitcnt lgkmcnt(10)
	v_mfma_f32_32x32x16_f16 v[4:19], v[144:147], v[40:43], v[4:19]
	v_exp_f32_e32 v60, v60
	v_exp_f32_e32 v61, v61
	v_exp_f32_e32 v62, v62
	v_exp_f32_e32 v63, v63
	s_waitcnt lgkmcnt(8)
	v_mfma_f32_32x32x16_f16 v[20:35], v[144:147], v[44:47], v[20:35]
	v_exp_f32_e32 v64, v64
	v_exp_f32_e32 v65, v65
	v_exp_f32_e32 v66, v66
	v_exp_f32_e32 v67, v67
	ds_read_b64_tr_b16 v[160:161], v212 offset:24576
	ds_read_b64_tr_b16 v[162:163], v212 offset:25088
	s_waitcnt lgkmcnt(9)
	v_mfma_f32_32x32x16_bf16 v[68:83], v[48:51], v[140:143], -4.0
	v_cvt_pk_f16_f32 v124, v84, v85
	v_pk_add_f16 v0, v0, v146
	v_pk_add_f16 v116, v166, v147
	v_cvt_pk_f16_f32 v125, v86, v87
	ds_read_b64_tr_b16 v[84:85], v212 offset:28672
	ds_read_b64_tr_b16 v[86:87], v212 offset:29184
	s_waitcnt lgkmcnt(10)
	v_mfma_f32_32x32x16_bf16 v[36:51], v[108:111], v[140:143], -4.0
	s_nop 0
	v_pk_add_f16 v0, v0, v124
	v_pk_add_f16 v108, v116, v125
	v_cvt_pk_f16_f32 v126, v88, v89
	v_cvt_pk_f16_f32 v127, v90, v91
	ds_read_b64_tr_b16 v[88:89], v212 offset:25600
	ds_read_b64_tr_b16 v[90:91], v212 offset:26112
	s_waitcnt lgkmcnt(11)
	v_mfma_f32_32x32x16_bf16 v[68:83], v[112:115], v[128:131], v[68:83]
	v_pk_add_f16 v0, v0, v126
	v_pk_add_f16 v108, v108, v127
	v_cvt_pk_f16_f32 v120, v92, v93
	v_cvt_pk_f16_f32 v121, v94, v95
	ds_read_b64_tr_b16 v[92:93], v212 offset:29696
	ds_read_b64_tr_b16 v[94:95], v212 offset:30208
	s_waitcnt lgkmcnt(12)
	v_mfma_f32_32x32x16_bf16 v[36:51], v[148:151], v[128:131], v[36:51]
	s_nop 0
	v_pk_add_f16 v0, v0, v120
	v_pk_add_f16 v108, v108, v121
	v_cvt_pk_f16_f32 v122, v96, v97
	v_cvt_pk_f16_f32 v123, v98, v99
	ds_read_b64_tr_b16 v[96:97], v212 offset:26624
	ds_read_b64_tr_b16 v[98:99], v212 offset:27136
	s_waitcnt lgkmcnt(13)
	v_mfma_f32_32x32x16_bf16 v[68:83], v[100:103], v[136:139], v[68:83]
	v_cvt_pk_f16_f32 v116, v52, v53
	v_pk_add_f16 v0, v0, v122
	v_pk_add_f16 v100, v108, v123
	v_cvt_pk_f16_f32 v117, v54, v55
	ds_read_b64_tr_b16 v[52:53], v212 offset:30720
	ds_read_b64_tr_b16 v[54:55], v212 offset:31232
	s_waitcnt lgkmcnt(14)
	v_mfma_f32_32x32x16_bf16 v[36:51], v[152:155], v[136:139], v[36:51]
	s_nop 0
	v_pk_add_f16 v0, v0, v116
	v_pk_add_f16 v100, v100, v117
	v_cvt_pk_f16_f32 v118, v56, v57
	v_cvt_pk_f16_f32 v119, v58, v59
	ds_read_b64_tr_b16 v[56:57], v212 offset:27648
	ds_read_b64_tr_b16 v[58:59], v212 offset:28160
	s_waitcnt lgkmcnt(14)
	v_mfma_f32_32x32x16_bf16 v[68:83], v[104:107], v[132:135], v[68:83]
	v_pk_add_f16 v0, v0, v118
	v_pk_add_f16 v100, v100, v119
	v_cvt_pk_f16_f32 v144, v60, v61
	v_cvt_pk_f16_f32 v145, v62, v63
	ds_read_b64_tr_b16 v[60:61], v212 offset:31744
	ds_read_b64_tr_b16 v[62:63], v212 offset:32256
	v_mfma_f32_32x32x16_bf16 v[36:51], v[156:159], v[132:135], v[36:51]
	s_nop 0
	v_pk_add_f16 v0, v0, v144
	v_pk_add_f16 v166, v100, v145
	v_cvt_pk_f16_f32 v146, v64, v65
	v_cvt_pk_f16_f32 v147, v66, v67
	s_add_u32 s54, s88, 0xbf4000
	s_addc_u32 s55, s89, 0
	s_add_i32 s10, s44, 0x6000
	s_mov_b32 m0, s10
	s_nop 0
	global_load_lds_dwordx4 v165, s[54:55]
	s_add_u32 s54, s14, 0xbdc000
	s_addc_u32 s55, s15, 0
	s_add_i32 s10, s44, 0xe000
	s_mov_b32 m0, s10
	s_nop 0
	global_load_lds_dwordx4 v164, s[54:55]
	s_waitcnt lgkmcnt(14)
	v_mfma_f32_32x32x16_f16 v[4:19], v[124:127], v[160:163], v[4:19]
	v_exp_f32_e32 v68, v68
	v_exp_f32_e32 v69, v69
	v_exp_f32_e32 v70, v70
	v_exp_f32_e32 v71, v71
	s_waitcnt lgkmcnt(12)
	v_mfma_f32_32x32x16_f16 v[20:35], v[124:127], v[84:87], v[20:35]
	v_exp_f32_e32 v72, v72
	v_exp_f32_e32 v73, v73
	v_exp_f32_e32 v74, v74
	v_exp_f32_e32 v75, v75
	ds_read_b128 v[64:67], v210 offset:40960
	ds_read_b128 v[104:107], v210 offset:41472
	s_waitcnt lgkmcnt(12)
	v_mfma_f32_32x32x16_f16 v[4:19], v[120:123], v[88:91], v[4:19]
	v_exp_f32_e32 v76, v76
	v_exp_f32_e32 v77, v77
	v_exp_f32_e32 v78, v78
	v_exp_f32_e32 v79, v79
	ds_read_b128 v[108:111], v210 offset:43008
	ds_read_b128 v[112:115], v210 offset:43520
	s_waitcnt lgkmcnt(12)
	v_mfma_f32_32x32x16_f16 v[20:35], v[120:123], v[92:95], v[20:35]
	v_exp_f32_e32 v80, v80
	v_exp_f32_e32 v81, v81
	v_exp_f32_e32 v82, v82
	v_exp_f32_e32 v83, v83
	ds_read_b128 v[148:151], v210 offset:45056
	ds_read_b128 v[152:155], v210 offset:45568
	s_waitcnt lgkmcnt(12)
	v_mfma_f32_32x32x16_f16 v[4:19], v[116:119], v[96:99], v[4:19]
	v_exp_f32_e32 v36, v36
	v_exp_f32_e32 v37, v37
	v_exp_f32_e32 v38, v38
	v_exp_f32_e32 v39, v39
	ds_read_b128 v[156:159], v210 offset:47104
	ds_read_b128 v[100:103], v210 offset:47616
	s_waitcnt lgkmcnt(12)
	v_mfma_f32_32x32x16_f16 v[20:35], v[116:119], v[52:55], v[20:35]
	v_exp_f32_e32 v40, v40
	v_exp_f32_e32 v41, v41
	v_exp_f32_e32 v42, v42
	v_exp_f32_e32 v43, v43
	s_waitcnt lgkmcnt(10)
	v_mfma_f32_32x32x16_f16 v[4:19], v[144:147], v[56:59], v[4:19]
	v_exp_f32_e32 v44, v44
	v_exp_f32_e32 v45, v45
	v_exp_f32_e32 v46, v46
	v_exp_f32_e32 v47, v47
	s_waitcnt lgkmcnt(8)
	v_mfma_f32_32x32x16_f16 v[20:35], v[144:147], v[60:63], v[20:35]
	v_exp_f32_e32 v48, v48
	v_exp_f32_e32 v49, v49
	v_exp_f32_e32 v50, v50
	v_exp_f32_e32 v51, v51
	s_waitcnt vmcnt(4) lgkmcnt(0)
	s_barrier
	ds_read_b64_tr_b16 v[160:161], v212 offset:32768
	ds_read_b64_tr_b16 v[162:163], v212 offset:33280
	s_waitcnt lgkmcnt(9)
	v_mfma_f32_32x32x16_bf16 v[84:99], v[64:67], v[140:143], -4.0
	v_mov_b32_e32 v116, v3
	v_pk_add_f16 v0, v0, v146
	v_pk_add_f16 v52, v166, v147
	v_cvt_pk_f16_f32 v124, v68, v69
	v_pk_add_f16 v0, v0, v52
	v_cvt_pk_f16_f32 v125, v70, v71
	v_dot2c_f32_f16_e32 v2, 0x3c003c00, v0
	v_mov_b32_e32 v0, v3
	ds_read_b64_tr_b16 v[68:69], v212 offset:36864
	ds_read_b64_tr_b16 v[70:71], v212 offset:37376
	s_waitcnt lgkmcnt(10)
	v_mfma_f32_32x32x16_bf16 v[52:67], v[104:107], v[140:143], -4.0
	s_nop 0
	v_pk_add_f16 v0, v0, v124
	v_pk_add_f16 v104, v116, v125
	v_cvt_pk_f16_f32 v126, v72, v73
	v_cvt_pk_f16_f32 v127, v74, v75
	ds_read_b64_tr_b16 v[72:73], v212 offset:33792
	ds_read_b64_tr_b16 v[74:75], v212 offset:34304
	s_waitcnt lgkmcnt(11)
	v_mfma_f32_32x32x16_bf16 v[84:99], v[108:111], v[128:131], v[84:99]
	v_pk_add_f16 v0, v0, v126
	v_pk_add_f16 v104, v104, v127
	v_cvt_pk_f16_f32 v120, v76, v77
	v_cvt_pk_f16_f32 v121, v78, v79
	ds_read_b64_tr_b16 v[76:77], v212 offset:37888
	ds_read_b64_tr_b16 v[78:79], v212 offset:38400
	s_waitcnt lgkmcnt(12)
	v_mfma_f32_32x32x16_bf16 v[52:67], v[112:115], v[128:131], v[52:67]
	v_pk_add_f16 v0, v0, v120
	v_pk_add_f16 v104, v104, v121
	v_cvt_pk_f16_f32 v122, v80, v81
	v_cvt_pk_f16_f32 v123, v82, v83
	ds_read_b64_tr_b16 v[80:81], v212 offset:34816
	ds_read_b64_tr_b16 v[82:83], v212 offset:35328
	s_waitcnt lgkmcnt(13)
	v_mfma_f32_32x32x16_bf16 v[84:99], v[148:151], v[136:139], v[84:99]
	v_pk_add_f16 v0, v0, v122
	v_pk_add_f16 v104, v104, v123
	v_cvt_pk_f16_f32 v116, v36, v37
	v_cvt_pk_f16_f32 v117, v38, v39
	ds_read_b64_tr_b16 v[36:37], v212 offset:38912
	ds_read_b64_tr_b16 v[38:39], v212 offset:39424
	s_waitcnt lgkmcnt(14)
	v_mfma_f32_32x32x16_bf16 v[52:67], v[152:155], v[136:139], v[52:67]
	v_pk_add_f16 v0, v0, v116
	v_pk_add_f16 v104, v104, v117
	v_cvt_pk_f16_f32 v118, v40, v41
	v_cvt_pk_f16_f32 v119, v42, v43
	ds_read_b64_tr_b16 v[40:41], v212 offset:35840
	ds_read_b64_tr_b16 v[42:43], v212 offset:36352
	s_waitcnt lgkmcnt(14)
	v_mfma_f32_32x32x16_bf16 v[84:99], v[156:159], v[132:135], v[84:99]
	v_pk_add_f16 v0, v0, v118
	v_pk_add_f16 v104, v104, v119
	v_cvt_pk_f16_f32 v144, v44, v45
	v_cvt_pk_f16_f32 v145, v46, v47
	ds_read_b64_tr_b16 v[44:45], v212 offset:39936
	ds_read_b64_tr_b16 v[46:47], v212 offset:40448
	v_mfma_f32_32x32x16_bf16 v[52:67], v[100:103], v[132:135], v[52:67]
	v_pk_add_f16 v0, v0, v144
	v_pk_add_f16 v165, v104, v145
	v_cvt_pk_f16_f32 v146, v48, v49
	v_cvt_pk_f16_f32 v147, v50, v51
	s_add_u32 s54, s14, 0xbe8000
	s_addc_u32 s55, s15, 0
	s_add_i32 s10, s44, 0x10000
	s_mov_b32 m0, s10
	s_nop 0
	global_load_lds_dwordx4 v164, s[54:55]
	s_waitcnt lgkmcnt(14)
	v_mfma_f32_32x32x16_f16 v[4:19], v[124:127], v[160:163], v[4:19]
	v_exp_f32_e32 v84, v84
	v_exp_f32_e32 v85, v85
	v_exp_f32_e32 v86, v86
	v_exp_f32_e32 v87, v87
	s_waitcnt lgkmcnt(12)
	v_mfma_f32_32x32x16_f16 v[20:35], v[124:127], v[68:71], v[20:35]
	v_exp_f32_e32 v88, v88
	v_exp_f32_e32 v89, v89
	v_exp_f32_e32 v90, v90
	v_exp_f32_e32 v91, v91
	ds_read_b128 v[48:51], v210
	ds_read_b128 v[100:103], v210 offset:512
	s_waitcnt lgkmcnt(12)
	v_mfma_f32_32x32x16_f16 v[4:19], v[120:123], v[72:75], v[4:19]
	v_exp_f32_e32 v92, v92
	v_exp_f32_e32 v93, v93
	v_exp_f32_e32 v94, v94
	v_exp_f32_e32 v95, v95
	ds_read_b128 v[104:107], v210 offset:2048
	ds_read_b128 v[108:111], v210 offset:2560
	s_waitcnt lgkmcnt(12)
	v_mfma_f32_32x32x16_f16 v[20:35], v[120:123], v[76:79], v[20:35]
	v_exp_f32_e32 v96, v96
	v_exp_f32_e32 v97, v97
	v_exp_f32_e32 v98, v98
	v_exp_f32_e32 v99, v99
	ds_read_b128 v[112:115], v210 offset:4096
	ds_read_b128 v[148:151], v210 offset:4608
	s_waitcnt lgkmcnt(12)
	v_mfma_f32_32x32x16_f16 v[4:19], v[116:119], v[80:83], v[4:19]
	v_exp_f32_e32 v52, v52
	v_exp_f32_e32 v53, v53
	v_exp_f32_e32 v54, v54
	v_exp_f32_e32 v55, v55
	ds_read_b128 v[152:155], v210 offset:6144
	ds_read_b128 v[156:159], v210 offset:6656
	s_waitcnt lgkmcnt(12)
	v_mfma_f32_32x32x16_f16 v[20:35], v[116:119], v[36:39], v[20:35]
	v_exp_f32_e32 v56, v56
	v_exp_f32_e32 v57, v57
	v_exp_f32_e32 v58, v58
	v_exp_f32_e32 v59, v59
	s_waitcnt lgkmcnt(10)
	v_mfma_f32_32x32x16_f16 v[4:19], v[144:147], v[40:43], v[4:19]
	v_exp_f32_e32 v60, v60
	v_exp_f32_e32 v61, v61
	v_exp_f32_e32 v62, v62
	v_exp_f32_e32 v63, v63
	s_waitcnt lgkmcnt(8)
	v_mfma_f32_32x32x16_f16 v[20:35], v[144:147], v[44:47], v[20:35]
	v_exp_f32_e32 v64, v64
	v_exp_f32_e32 v65, v65
	v_exp_f32_e32 v66, v66
	v_exp_f32_e32 v67, v67
	ds_read_b64_tr_b16 v[160:161], v212 offset:40960
	ds_read_b64_tr_b16 v[162:163], v212 offset:41472
	s_waitcnt lgkmcnt(9)
	v_mfma_f32_32x32x16_bf16 v[68:83], v[48:51], v[140:143], -4.0
	v_cvt_pk_f16_f32 v124, v84, v85
	v_pk_add_f16 v0, v0, v146
	v_pk_add_f16 v116, v165, v147
	v_cvt_pk_f16_f32 v125, v86, v87
	ds_read_b64_tr_b16 v[84:85], v212 offset:45056
	ds_read_b64_tr_b16 v[86:87], v212 offset:45568
	s_waitcnt lgkmcnt(10)
	v_mfma_f32_32x32x16_bf16 v[36:51], v[100:103], v[140:143], -4.0
	s_nop 0
	v_pk_add_f16 v0, v0, v124
	v_pk_add_f16 v100, v116, v125
	v_cvt_pk_f16_f32 v126, v88, v89
	v_cvt_pk_f16_f32 v127, v90, v91
	ds_read_b64_tr_b16 v[88:89], v212 offset:41984
	ds_read_b64_tr_b16 v[90:91], v212 offset:42496
	s_waitcnt lgkmcnt(11)
	v_mfma_f32_32x32x16_bf16 v[68:83], v[104:107], v[128:131], v[68:83]
	v_pk_add_f16 v0, v0, v126
	v_pk_add_f16 v100, v100, v127
	v_cvt_pk_f16_f32 v120, v92, v93
	v_cvt_pk_f16_f32 v121, v94, v95
	ds_read_b64_tr_b16 v[92:93], v212 offset:46080
	ds_read_b64_tr_b16 v[94:95], v212 offset:46592
	s_waitcnt lgkmcnt(12)
	v_mfma_f32_32x32x16_bf16 v[36:51], v[108:111], v[128:131], v[36:51]
	s_nop 0
	v_pk_add_f16 v0, v0, v120
	v_pk_add_f16 v100, v100, v121
	v_cvt_pk_f16_f32 v122, v96, v97
	v_cvt_pk_f16_f32 v123, v98, v99
	ds_read_b64_tr_b16 v[96:97], v212 offset:43008
	ds_read_b64_tr_b16 v[98:99], v212 offset:43520
	s_waitcnt lgkmcnt(13)
	v_mfma_f32_32x32x16_bf16 v[68:83], v[112:115], v[136:139], v[68:83]
	v_pk_add_f16 v0, v0, v122
	v_pk_add_f16 v100, v100, v123
	v_cvt_pk_f16_f32 v116, v52, v53
	v_cvt_pk_f16_f32 v117, v54, v55
	ds_read_b64_tr_b16 v[52:53], v212 offset:47104
	ds_read_b64_tr_b16 v[54:55], v212 offset:47616
	s_waitcnt lgkmcnt(14)
	v_mfma_f32_32x32x16_bf16 v[36:51], v[148:151], v[136:139], v[36:51]
	s_nop 0
	v_pk_add_f16 v0, v0, v116
	v_pk_add_f16 v100, v100, v117
	v_cvt_pk_f16_f32 v118, v56, v57
	v_cvt_pk_f16_f32 v119, v58, v59
	ds_read_b64_tr_b16 v[56:57], v212 offset:44032
	ds_read_b64_tr_b16 v[58:59], v212 offset:44544
	s_waitcnt lgkmcnt(14)
	v_mfma_f32_32x32x16_bf16 v[68:83], v[152:155], v[132:135], v[68:83]
	v_pk_add_f16 v0, v0, v118
	v_pk_add_f16 v100, v100, v119
	v_cvt_pk_f16_f32 v144, v60, v61
	v_cvt_pk_f16_f32 v145, v62, v63
	ds_read_b64_tr_b16 v[60:61], v212 offset:48128
	ds_read_b64_tr_b16 v[62:63], v212 offset:48640
	v_mfma_f32_32x32x16_bf16 v[36:51], v[156:159], v[132:135], v[36:51]
	s_nop 0
	v_pk_add_f16 v0, v0, v144
	v_pk_add_f16 v165, v100, v145
	v_cvt_pk_f16_f32 v146, v64, v65
	v_cvt_pk_f16_f32 v147, v66, v67
	s_add_u32 s14, s14, 0xbf4000
	s_addc_u32 s15, s15, 0
	s_add_i32 s44, s44, 0x12000
	s_mov_b32 m0, s44
	s_nop 0
	global_load_lds_dwordx4 v164, s[14:15]
	s_waitcnt lgkmcnt(14)
	v_mfma_f32_32x32x16_f16 v[4:19], v[124:127], v[160:163], v[4:19]
	v_exp_f32_e32 v68, v68
	v_exp_f32_e32 v69, v69
	v_exp_f32_e32 v70, v70
	v_exp_f32_e32 v71, v71
	s_waitcnt lgkmcnt(12)
	v_mfma_f32_32x32x16_f16 v[20:35], v[124:127], v[84:87], v[20:35]
	v_exp_f32_e32 v72, v72
	v_exp_f32_e32 v73, v73
	v_exp_f32_e32 v74, v74
	v_exp_f32_e32 v75, v75
	ds_read_b128 v[64:67], v210 offset:8192
	ds_read_b128 v[104:107], v210 offset:8704
	s_waitcnt lgkmcnt(12)
	v_mfma_f32_32x32x16_f16 v[4:19], v[120:123], v[88:91], v[4:19]
	v_exp_f32_e32 v76, v76
	v_exp_f32_e32 v77, v77
	v_exp_f32_e32 v78, v78
	v_exp_f32_e32 v79, v79
	ds_read_b128 v[108:111], v210 offset:10240
	ds_read_b128 v[112:115], v210 offset:10752
	s_waitcnt lgkmcnt(12)
	v_mfma_f32_32x32x16_f16 v[20:35], v[120:123], v[92:95], v[20:35]
	v_exp_f32_e32 v80, v80
	v_exp_f32_e32 v81, v81
	v_exp_f32_e32 v82, v82
	v_exp_f32_e32 v83, v83
	ds_read_b128 v[148:151], v210 offset:12288
	ds_read_b128 v[152:155], v210 offset:12800
	s_waitcnt lgkmcnt(12)
	v_mfma_f32_32x32x16_f16 v[4:19], v[116:119], v[96:99], v[4:19]
	v_exp_f32_e32 v36, v36
	v_exp_f32_e32 v37, v37
	v_exp_f32_e32 v38, v38
	v_exp_f32_e32 v39, v39
	ds_read_b128 v[156:159], v210 offset:14336
	ds_read_b128 v[100:103], v210 offset:14848
	s_waitcnt lgkmcnt(12)
	v_mfma_f32_32x32x16_f16 v[20:35], v[116:119], v[52:55], v[20:35]
	v_exp_f32_e32 v40, v40
	v_exp_f32_e32 v41, v41
	v_exp_f32_e32 v42, v42
	v_exp_f32_e32 v43, v43
	s_waitcnt lgkmcnt(10)
	v_mfma_f32_32x32x16_f16 v[4:19], v[144:147], v[56:59], v[4:19]
	v_exp_f32_e32 v44, v44
	v_exp_f32_e32 v45, v45
	v_exp_f32_e32 v46, v46
	v_exp_f32_e32 v47, v47
	s_waitcnt lgkmcnt(8)
	v_mfma_f32_32x32x16_f16 v[20:35], v[144:147], v[60:63], v[20:35]
	v_exp_f32_e32 v48, v48
	v_exp_f32_e32 v49, v49
	v_exp_f32_e32 v50, v50
	v_exp_f32_e32 v51, v51
	s_waitcnt vmcnt(2) lgkmcnt(0)
	s_barrier
	ds_read_b64_tr_b16 v[160:161], v211 offset:49152
	ds_read_b64_tr_b16 v[162:163], v211 offset:49664
	s_waitcnt lgkmcnt(9)
	v_mfma_f32_32x32x16_bf16 v[84:99], v[64:67], v[140:143], -4.0
	v_mov_b32_e32 v116, v3
	v_pk_add_f16 v0, v0, v146
	v_pk_add_f16 v52, v165, v147
	v_cvt_pk_f16_f32 v124, v68, v69
	v_pk_add_f16 v0, v0, v52
	v_cvt_pk_f16_f32 v125, v70, v71
	v_dot2c_f32_f16_e32 v2, 0x3c003c00, v0
	v_mov_b32_e32 v0, v3
	ds_read_b64_tr_b16 v[68:69], v211 offset:53248
	ds_read_b64_tr_b16 v[70:71], v211 offset:53760
	s_waitcnt lgkmcnt(10)
	v_mfma_f32_32x32x16_bf16 v[52:67], v[104:107], v[140:143], -4.0
	s_nop 0
	v_pk_add_f16 v0, v0, v124
	v_pk_add_f16 v104, v116, v125
	v_cvt_pk_f16_f32 v126, v72, v73
	v_cvt_pk_f16_f32 v127, v74, v75
	ds_read_b64_tr_b16 v[72:73], v211 offset:50176
	ds_read_b64_tr_b16 v[74:75], v211 offset:50688
	s_waitcnt lgkmcnt(11)
	v_mfma_f32_32x32x16_bf16 v[84:99], v[108:111], v[128:131], v[84:99]
	v_pk_add_f16 v0, v0, v126
	v_pk_add_f16 v104, v104, v127
	v_cvt_pk_f16_f32 v120, v76, v77
	v_cvt_pk_f16_f32 v121, v78, v79
	ds_read_b64_tr_b16 v[76:77], v211 offset:54272
	ds_read_b64_tr_b16 v[78:79], v211 offset:54784
	s_waitcnt lgkmcnt(12)
	v_mfma_f32_32x32x16_bf16 v[52:67], v[112:115], v[128:131], v[52:67]
	v_pk_add_f16 v0, v0, v120
	v_pk_add_f16 v104, v104, v121
	v_cvt_pk_f16_f32 v122, v80, v81
	v_cvt_pk_f16_f32 v123, v82, v83
	ds_read_b64_tr_b16 v[80:81], v211 offset:51200
	ds_read_b64_tr_b16 v[82:83], v211 offset:51712
	s_waitcnt lgkmcnt(13)
	v_mfma_f32_32x32x16_bf16 v[84:99], v[148:151], v[136:139], v[84:99]
	v_pk_add_f16 v0, v0, v122
	v_pk_add_f16 v104, v104, v123
	v_cvt_pk_f16_f32 v116, v36, v37
	v_cvt_pk_f16_f32 v117, v38, v39
	ds_read_b64_tr_b16 v[36:37], v211 offset:55296
	ds_read_b64_tr_b16 v[38:39], v211 offset:55808
	s_waitcnt lgkmcnt(14)
	v_mfma_f32_32x32x16_bf16 v[52:67], v[152:155], v[136:139], v[52:67]
	v_pk_add_f16 v0, v0, v116
	v_pk_add_f16 v104, v104, v117
	v_cvt_pk_f16_f32 v118, v40, v41
	v_cvt_pk_f16_f32 v119, v42, v43
	ds_read_b64_tr_b16 v[40:41], v211 offset:52224
	ds_read_b64_tr_b16 v[42:43], v211 offset:52736
	s_waitcnt lgkmcnt(14)
	v_mfma_f32_32x32x16_bf16 v[84:99], v[156:159], v[132:135], v[84:99]
	v_pk_add_f16 v0, v0, v118
	v_pk_add_f16 v104, v104, v119
	v_cvt_pk_f16_f32 v144, v44, v45
	v_cvt_pk_f16_f32 v145, v46, v47
	ds_read_b64_tr_b16 v[44:45], v211 offset:56320
	ds_read_b64_tr_b16 v[46:47], v211 offset:56832
	v_mfma_f32_32x32x16_bf16 v[52:67], v[100:103], v[132:135], v[52:67]
	v_pk_add_f16 v0, v0, v144
	v_pk_add_f16 v164, v104, v145
	v_cvt_pk_f16_f32 v146, v48, v49
	v_cvt_pk_f16_f32 v147, v50, v51
	s_waitcnt lgkmcnt(14)
	v_mfma_f32_32x32x16_f16 v[4:19], v[124:127], v[160:163], v[4:19]
	v_exp_f32_e32 v84, v84
	v_exp_f32_e32 v85, v85
	v_exp_f32_e32 v86, v86
	v_exp_f32_e32 v87, v87
	s_waitcnt lgkmcnt(12)
	v_mfma_f32_32x32x16_f16 v[20:35], v[124:127], v[68:71], v[20:35]
	v_exp_f32_e32 v88, v88
	v_exp_f32_e32 v89, v89
	v_exp_f32_e32 v90, v90
	v_exp_f32_e32 v91, v91
	ds_read_b128 v[48:51], v210 offset:16384
	ds_read_b128 v[100:103], v210 offset:16896
	s_waitcnt lgkmcnt(12)
	v_mfma_f32_32x32x16_f16 v[4:19], v[120:123], v[72:75], v[4:19]
	v_exp_f32_e32 v92, v92
	v_exp_f32_e32 v93, v93
	v_exp_f32_e32 v94, v94
	v_exp_f32_e32 v95, v95
	ds_read_b128 v[104:107], v210 offset:18432
	ds_read_b128 v[108:111], v210 offset:18944
	s_waitcnt lgkmcnt(12)
	v_mfma_f32_32x32x16_f16 v[20:35], v[120:123], v[76:79], v[20:35]
	v_exp_f32_e32 v96, v96
	v_exp_f32_e32 v97, v97
	v_exp_f32_e32 v98, v98
	v_exp_f32_e32 v99, v99
	ds_read_b128 v[112:115], v210 offset:20480
	ds_read_b128 v[148:151], v210 offset:20992
	s_waitcnt lgkmcnt(12)
	v_mfma_f32_32x32x16_f16 v[4:19], v[116:119], v[80:83], v[4:19]
	v_exp_f32_e32 v52, v52
	v_exp_f32_e32 v53, v53
	v_exp_f32_e32 v54, v54
	v_exp_f32_e32 v55, v55
	ds_read_b128 v[152:155], v210 offset:22528
	ds_read_b128 v[156:159], v210 offset:23040
	s_waitcnt lgkmcnt(12)
	v_mfma_f32_32x32x16_f16 v[20:35], v[116:119], v[36:39], v[20:35]
	v_exp_f32_e32 v56, v56
	v_exp_f32_e32 v57, v57
	v_exp_f32_e32 v58, v58
	v_exp_f32_e32 v59, v59
	s_waitcnt lgkmcnt(10)
	v_mfma_f32_32x32x16_f16 v[4:19], v[144:147], v[40:43], v[4:19]
	v_exp_f32_e32 v60, v60
	v_exp_f32_e32 v61, v61
	v_exp_f32_e32 v62, v62
	v_exp_f32_e32 v63, v63
	s_waitcnt lgkmcnt(8)
	v_mfma_f32_32x32x16_f16 v[20:35], v[144:147], v[44:47], v[20:35]
	v_exp_f32_e32 v64, v64
	v_exp_f32_e32 v65, v65
	v_exp_f32_e32 v66, v66
	v_exp_f32_e32 v67, v67
	ds_read_b64_tr_b16 v[160:161], v211 offset:57344
	ds_read_b64_tr_b16 v[162:163], v211 offset:57856
	s_waitcnt lgkmcnt(9)
	v_mfma_f32_32x32x16_bf16 v[68:83], v[48:51], v[140:143], -4.0
	v_cvt_pk_f16_f32 v124, v84, v85
	v_pk_add_f16 v0, v0, v146
	v_pk_add_f16 v116, v164, v147
	v_cvt_pk_f16_f32 v125, v86, v87
	ds_read_b64_tr_b16 v[84:85], v211 offset:61440
	ds_read_b64_tr_b16 v[86:87], v211 offset:61952
	s_waitcnt lgkmcnt(10)
	v_mfma_f32_32x32x16_bf16 v[36:51], v[100:103], v[140:143], -4.0
	s_nop 0
	v_pk_add_f16 v0, v0, v124
	v_pk_add_f16 v100, v116, v125
	v_cvt_pk_f16_f32 v126, v88, v89
	v_cvt_pk_f16_f32 v127, v90, v91
	ds_read_b64_tr_b16 v[88:89], v211 offset:58368
	ds_read_b64_tr_b16 v[90:91], v211 offset:58880
	s_waitcnt lgkmcnt(11)
	v_mfma_f32_32x32x16_bf16 v[68:83], v[104:107], v[128:131], v[68:83]
	v_pk_add_f16 v0, v0, v126
	v_pk_add_f16 v100, v100, v127
	v_cvt_pk_f16_f32 v120, v92, v93
	v_cvt_pk_f16_f32 v121, v94, v95
	ds_read_b64_tr_b16 v[92:93], v211 offset:62464
	ds_read_b64_tr_b16 v[94:95], v211 offset:62976
	s_waitcnt lgkmcnt(12)
	v_mfma_f32_32x32x16_bf16 v[36:51], v[108:111], v[128:131], v[36:51]
	s_nop 0
	v_pk_add_f16 v0, v0, v120
	v_pk_add_f16 v100, v100, v121
	v_cvt_pk_f16_f32 v122, v96, v97
	v_cvt_pk_f16_f32 v123, v98, v99
	ds_read_b64_tr_b16 v[96:97], v211 offset:59392
	ds_read_b64_tr_b16 v[98:99], v211 offset:59904
	s_waitcnt lgkmcnt(13)
	v_mfma_f32_32x32x16_bf16 v[68:83], v[112:115], v[136:139], v[68:83]
	v_pk_add_f16 v0, v0, v122
	v_pk_add_f16 v100, v100, v123
	v_cvt_pk_f16_f32 v116, v52, v53
	v_cvt_pk_f16_f32 v117, v54, v55
	ds_read_b64_tr_b16 v[52:53], v211 offset:63488
	ds_read_b64_tr_b16 v[54:55], v211 offset:64000
	s_waitcnt lgkmcnt(14)
	v_mfma_f32_32x32x16_bf16 v[36:51], v[148:151], v[136:139], v[36:51]
	s_nop 0
	v_pk_add_f16 v0, v0, v116
	v_pk_add_f16 v100, v100, v117
	v_cvt_pk_f16_f32 v118, v56, v57
	v_cvt_pk_f16_f32 v119, v58, v59
	ds_read_b64_tr_b16 v[56:57], v211 offset:60416
	ds_read_b64_tr_b16 v[58:59], v211 offset:60928
	s_waitcnt lgkmcnt(14)
	v_mfma_f32_32x32x16_bf16 v[68:83], v[152:155], v[132:135], v[68:83]
	v_pk_add_f16 v0, v0, v118
	v_pk_add_f16 v100, v100, v119
	v_cvt_pk_f16_f32 v144, v60, v61
	v_cvt_pk_f16_f32 v145, v62, v63
	ds_read_b64_tr_b16 v[60:61], v211 offset:64512
	ds_read_b64_tr_b16 v[62:63], v211 offset:65024
	v_mfma_f32_32x32x16_bf16 v[36:51], v[156:159], v[132:135], v[36:51]
	s_nop 0
	v_pk_add_f16 v0, v0, v144
	v_pk_add_f16 v164, v100, v145
	v_cvt_pk_f16_f32 v146, v64, v65
	v_cvt_pk_f16_f32 v147, v66, v67
	s_waitcnt lgkmcnt(14)
	v_mfma_f32_32x32x16_f16 v[4:19], v[124:127], v[160:163], v[4:19]
	v_exp_f32_e32 v68, v68
	v_exp_f32_e32 v69, v69
	v_exp_f32_e32 v70, v70
	v_exp_f32_e32 v71, v71
	s_waitcnt lgkmcnt(12)
	v_mfma_f32_32x32x16_f16 v[20:35], v[124:127], v[84:87], v[20:35]
	v_exp_f32_e32 v72, v72
	v_exp_f32_e32 v73, v73
	v_exp_f32_e32 v74, v74
	v_exp_f32_e32 v75, v75
	ds_read_b128 v[84:87], v210 offset:24576
	ds_read_b128 v[104:107], v210 offset:25088
	s_waitcnt lgkmcnt(12)
	v_mfma_f32_32x32x16_f16 v[4:19], v[120:123], v[88:91], v[4:19]
	v_exp_f32_e32 v76, v76
	v_exp_f32_e32 v77, v77
	v_exp_f32_e32 v78, v78
	v_exp_f32_e32 v79, v79
	ds_read_b128 v[108:111], v210 offset:26624
	ds_read_b128 v[112:115], v210 offset:27136
	s_waitcnt lgkmcnt(12)
	v_mfma_f32_32x32x16_f16 v[20:35], v[120:123], v[92:95], v[20:35]
	v_exp_f32_e32 v80, v80
	v_exp_f32_e32 v81, v81
	v_exp_f32_e32 v82, v82
	v_exp_f32_e32 v83, v83
	ds_read_b128 v[148:151], v210 offset:28672
	ds_read_b128 v[152:155], v210 offset:29184
	s_waitcnt lgkmcnt(12)
	v_mfma_f32_32x32x16_f16 v[4:19], v[116:119], v[96:99], v[4:19]
	v_exp_f32_e32 v36, v36
	v_exp_f32_e32 v37, v37
	v_exp_f32_e32 v38, v38
	v_exp_f32_e32 v39, v39
	ds_read_b128 v[156:159], v210 offset:30720
	ds_read_b128 v[160:163], v210 offset:31232
	s_waitcnt lgkmcnt(12)
	v_mfma_f32_32x32x16_f16 v[20:35], v[116:119], v[52:55], v[20:35]
	v_exp_f32_e32 v40, v40
	v_exp_f32_e32 v41, v41
	v_exp_f32_e32 v42, v42
	v_exp_f32_e32 v43, v43
	s_waitcnt lgkmcnt(10)
	v_mfma_f32_32x32x16_f16 v[4:19], v[144:147], v[56:59], v[4:19]
	v_exp_f32_e32 v44, v44
	v_exp_f32_e32 v45, v45
	v_exp_f32_e32 v46, v46
	v_exp_f32_e32 v47, v47
	s_waitcnt lgkmcnt(8)
	v_mfma_f32_32x32x16_f16 v[20:35], v[144:147], v[60:63], v[20:35]
	v_exp_f32_e32 v48, v48
	v_exp_f32_e32 v49, v49
	v_exp_f32_e32 v50, v50
	v_exp_f32_e32 v51, v51
	s_waitcnt vmcnt(0) lgkmcnt(0)
	s_barrier
	ds_read_b64_tr_b16 v[100:101], v212 offset:16384
	ds_read_b64_tr_b16 v[102:103], v212 offset:16896
	s_waitcnt lgkmcnt(9)
	v_mfma_f32_32x32x16_bf16 v[52:67], v[84:87], v[140:143], -4.0
	v_mov_b32_e32 v116, v3
	v_pk_add_f16 v0, v0, v146
	v_pk_add_f16 v84, v164, v147
	v_cvt_pk_f16_f32 v124, v68, v69
	v_pk_add_f16 v0, v0, v84
	v_cvt_pk_f16_f32 v125, v70, v71
	v_dot2c_f32_f16_e32 v2, 0x3c003c00, v0
	v_mov_b32_e32 v0, v3
	ds_read_b64_tr_b16 v[68:69], v212 offset:20480
	ds_read_b64_tr_b16 v[70:71], v212 offset:20992
	s_waitcnt lgkmcnt(10)
	v_mfma_f32_32x32x16_bf16 v[84:99], v[104:107], v[140:143], -4.0
	s_nop 0
	v_pk_add_f16 v0, v0, v124
	v_pk_add_f16 v104, v116, v125
	v_cvt_pk_f16_f32 v126, v72, v73
	v_cvt_pk_f16_f32 v127, v74, v75
	ds_read_b64_tr_b16 v[72:73], v212 offset:17408
	ds_read_b64_tr_b16 v[74:75], v212 offset:17920
	s_waitcnt lgkmcnt(11)
	v_mfma_f32_32x32x16_bf16 v[52:67], v[108:111], v[128:131], v[52:67]
	v_pk_add_f16 v0, v0, v126
	v_pk_add_f16 v104, v104, v127
	v_cvt_pk_f16_f32 v120, v76, v77
	v_cvt_pk_f16_f32 v121, v78, v79
	ds_read_b64_tr_b16 v[76:77], v212 offset:21504
	ds_read_b64_tr_b16 v[78:79], v212 offset:22016
	s_waitcnt lgkmcnt(12)
	v_mfma_f32_32x32x16_bf16 v[84:99], v[112:115], v[128:131], v[84:99]
	v_pk_add_f16 v0, v0, v120
	v_pk_add_f16 v104, v104, v121
	v_cvt_pk_f16_f32 v122, v80, v81
	v_cvt_pk_f16_f32 v123, v82, v83
	ds_read_b64_tr_b16 v[80:81], v212 offset:18432
	ds_read_b64_tr_b16 v[82:83], v212 offset:18944
	s_waitcnt lgkmcnt(13)
	v_mfma_f32_32x32x16_bf16 v[52:67], v[148:151], v[136:139], v[52:67]
	v_pk_add_f16 v0, v0, v122
	v_pk_add_f16 v104, v104, v123
	v_cvt_pk_f16_f32 v116, v36, v37
	v_cvt_pk_f16_f32 v117, v38, v39
	ds_read_b64_tr_b16 v[36:37], v212 offset:22528
	ds_read_b64_tr_b16 v[38:39], v212 offset:23040
	s_waitcnt lgkmcnt(14)
	v_mfma_f32_32x32x16_bf16 v[84:99], v[152:155], v[136:139], v[84:99]
	v_pk_add_f16 v0, v0, v116
	v_pk_add_f16 v104, v104, v117
	v_cvt_pk_f16_f32 v118, v40, v41
	v_cvt_pk_f16_f32 v119, v42, v43
	ds_read_b64_tr_b16 v[40:41], v212 offset:19456
	ds_read_b64_tr_b16 v[42:43], v212 offset:19968
	s_waitcnt lgkmcnt(14)
	v_mfma_f32_32x32x16_bf16 v[52:67], v[156:159], v[132:135], v[52:67]
	v_pk_add_f16 v0, v0, v118
	v_pk_add_f16 v104, v104, v119
	v_cvt_pk_f16_f32 v144, v44, v45
	v_cvt_pk_f16_f32 v145, v46, v47
	ds_read_b64_tr_b16 v[44:45], v212 offset:23552
	ds_read_b64_tr_b16 v[46:47], v212 offset:24064
	v_mfma_f32_32x32x16_bf16 v[84:99], v[160:163], v[132:135], v[84:99]
	v_pk_add_f16 v0, v0, v144
	v_pk_add_f16 v104, v104, v145
	v_cvt_pk_f16_f32 v146, v48, v49
	v_cvt_pk_f16_f32 v147, v50, v51
	s_nop 0
	v_exp_f32_e32 v52, v52
	v_exp_f32_e32 v53, v53
	v_exp_f32_e32 v54, v54
	v_exp_f32_e32 v55, v55
	s_nop 0
	v_exp_f32_e32 v56, v56
	v_exp_f32_e32 v57, v57
	v_exp_f32_e32 v58, v58
	v_exp_f32_e32 v59, v59
	s_nop 0
	v_exp_f32_e32 v60, v60
	v_exp_f32_e32 v61, v61
	v_exp_f32_e32 v62, v62
	v_exp_f32_e32 v63, v63
	s_nop 0
	v_exp_f32_e32 v64, v64
	v_exp_f32_e32 v65, v65
	v_exp_f32_e32 v66, v66
	v_exp_f32_e32 v67, v67
	v_exp_f32_e32 v84, v84
	v_exp_f32_e32 v85, v85
	v_exp_f32_e32 v86, v86
	v_exp_f32_e32 v87, v87
	s_nop 0
	v_exp_f32_e32 v88, v88
	v_exp_f32_e32 v89, v89
	v_exp_f32_e32 v90, v90
	v_exp_f32_e32 v91, v91
	s_nop 0
	v_exp_f32_e32 v92, v92
	v_exp_f32_e32 v93, v93
	v_exp_f32_e32 v94, v94
	v_exp_f32_e32 v95, v95
	s_nop 0
	v_exp_f32_e32 v96, v96
	v_exp_f32_e32 v97, v97
	v_exp_f32_e32 v98, v98
	v_exp_f32_e32 v99, v99
	s_waitcnt lgkmcnt(14)
	v_mfma_f32_32x32x16_f16 v[4:19], v[124:127], v[100:103], v[4:19]
	v_pk_add_f16 v0, v0, v146
	v_cvt_pk_f16_f32 v48, v52, v53
	v_cvt_pk_f16_f32 v52, v60, v61
	v_cvt_pk_f16_f32 v49, v54, v55
	v_cvt_pk_f16_f32 v50, v56, v57
	v_cvt_pk_f16_f32 v54, v64, v65
	v_cvt_pk_f16_f32 v56, v84, v85
	s_waitcnt lgkmcnt(12)
	v_mfma_f32_32x32x16_f16 v[20:35], v[124:127], v[68:71], v[20:35]
	v_pk_add_f16 v68, v104, v147
	v_cvt_pk_f16_f32 v60, v92, v93
	v_pk_add_f16 v0, v0, v48
	v_pk_add_f16 v64, v68, v52
	v_cvt_pk_f16_f32 v53, v62, v63
	v_pk_add_f16 v0, v0, v56
	v_pk_add_f16 v64, v64, v60
	s_waitcnt lgkmcnt(10)
	v_mfma_f32_32x32x16_f16 v[4:19], v[120:123], v[72:75], v[4:19]
	v_cvt_pk_f16_f32 v57, v86, v87
	v_cvt_pk_f16_f32 v61, v94, v95
	v_pk_add_f16 v0, v0, v49
	v_cvt_pk_f16_f32 v51, v58, v59
	v_pk_add_f16 v0, v0, v57
	v_cvt_pk_f16_f32 v58, v88, v89
	v_cvt_pk_f16_f32 v62, v96, v97
	s_waitcnt lgkmcnt(8)
	v_mfma_f32_32x32x16_f16 v[20:35], v[120:123], v[76:79], v[20:35]
	v_pk_add_f16 v0, v0, v50
	v_cvt_pk_f16_f32 v55, v66, v67
	v_pk_add_f16 v0, v0, v58
	v_cvt_pk_f16_f32 v59, v90, v91
	v_cvt_pk_f16_f32 v63, v98, v99
	v_pk_add_f16 v0, v0, v51
	s_waitcnt lgkmcnt(6)
	v_mfma_f32_32x32x16_f16 v[4:19], v[116:119], v[80:83], v[4:19]
	v_pk_add_f16 v0, v0, v59
	s_waitcnt lgkmcnt(4)
	v_mfma_f32_32x32x16_f16 v[20:35], v[116:119], v[36:39], v[20:35]
	v_pk_add_f16 v36, v64, v53
	s_nop 0
	v_pk_add_f16 v36, v36, v61
	s_nop 0
	v_pk_add_f16 v36, v36, v54
	s_nop 0
	v_pk_add_f16 v36, v36, v62
	s_waitcnt lgkmcnt(2)
	v_mfma_f32_32x32x16_f16 v[4:19], v[144:147], v[40:43], v[4:19]
	v_pk_add_f16 v36, v36, v55
	s_nop 0
	v_pk_add_f16 v36, v36, v63
	s_nop 0
	v_pk_add_f16 v0, v36, v0
	s_nop 0
	v_dot2c_f32_f16_e32 v2, 0x3c003c00, v0
	s_waitcnt lgkmcnt(0)
	v_mfma_f32_32x32x16_f16 v[20:35], v[144:147], v[44:47], v[20:35]
	ds_read_b64_tr_b16 v[36:37],v214 offset:0
	ds_read_b64_tr_b16 v[38:39],v214 offset:512
	ds_read_b64_tr_b16 v[40:41],v214 offset:1024
	ds_read_b64_tr_b16 v[42:43],v214 offset:1536
	ds_read_b64_tr_b16 v[44:45],v214 offset:2048
	ds_read_b64_tr_b16 v[46:47],v214 offset:2560
	ds_read_b64_tr_b16 v[64:65],v214 offset:3072
	ds_read_b64_tr_b16 v[66:67],v214 offset:3584
	s_waitcnt lgkmcnt(0)
	s_nop 0
	v_mfma_f32_32x32x16_f16 v[4:19], v[48:51], v[36:39], v[4:19]
	ds_read_b64_tr_b16 v[36:37],v214 offset:4096
	ds_read_b64_tr_b16 v[38:39],v214 offset:4608
	v_mfma_f32_32x32x16_f16 v[4:19], v[52:55], v[40:43], v[4:19]
	ds_read_b64_tr_b16 v[40:41],v214 offset:5120
	ds_read_b64_tr_b16 v[42:43],v214 offset:5632
	v_mfma_f32_32x32x16_f16 v[4:19], v[56:59], v[44:47], v[4:19]
	ds_read_b64_tr_b16 v[44:45],v214 offset:6144
	ds_read_b64_tr_b16 v[46:47],v214 offset:6656
	v_mfma_f32_32x32x16_f16 v[4:19], v[60:63], v[64:67], v[4:19]
	ds_read_b64_tr_b16 v[64:65],v214 offset:7168
	ds_read_b64_tr_b16 v[66:67],v214 offset:7680
	s_waitcnt lgkmcnt(0)
	v_mfma_f32_32x32x16_f16 v[20:35], v[48:51], v[36:39], v[20:35]
	v_mov_b32_e32 v36, v2
	s_nop 1
	v_permlane32_swap_b32_e32 v2, v36
	v_mfma_f32_32x32x16_f16 v[20:35], v[52:55], v[40:43], v[20:35]
	v_mfma_f32_32x32x16_f16 v[20:35], v[56:59], v[44:47], v[20:35]
	v_mfma_f32_32x32x16_f16 v[20:35], v[60:63], v[64:67], v[20:35]
	s_and_saveexec_b64 s[14:15], s[4:5]
	s_cbranch_execz .LBB0_241
	v_add_f32_e32 v0, v2, v36
	v_lshl_add_u32 v2, v207, 2, s11
	ds_write_b32 v2, v0 offset:128
	s_branch .LBB0_241
